# router k-loop: waves 4-7 enter 384 cycles later so SIMD partners do not wait on memory at the same time
# speedup vs baseline: 1.0015x; 1.0015x over previous
; __device__ __forceinline__ void p7_ffn_prep(const Ctx& C, bool dummy = false) {
;     ...
;     for (int u = C.bid; u < T_ / 128; u += C.G) {
;         if (C.tid < 32) cnt[C.tid] = 0;
;         __syncthreads();
;         const int row = u * 128 + C.wave * 16 + i;
;         float ssq = 0.f; { const f32x4* rp = (const f32x4*)(WSP(float, WS_ROWSS) + (size_t)row * 32);
; #pragma unroll
;           for (int k = 0; k < 8; ++k) { const f32x4 v = rp[k]; ssq += (v[0] + v[1]) + (v[2] + v[3]); } }
;         const float rstd = rsqrtf(ssq * (1.0f / D_) + EPS);
;         const _Float16* __restrict__ x1 = WSP(_Float16, WS_X1H) + (size_t)row * D_ + 8 * g4; const float* fg = C.ka->in[I_FFG] + 8 * g4; unsigned char* __restrict__ h2 = WSP(unsigned char, WS_H) + (size_t)row * D_ + 8 * g4;
;         f32x4 a0 = {0.f, 0.f, 0.f, 0.f}, a1 = {0.f, 0.f, 0.f, 0.f};
;         const int rot = ((C.bid >> 3) * 2 + (C.bid & 1)) & 63;
;     ...
;         f16x8 xq[4];
; #pragma unroll
;         for (int d = 0; d < 4; ++d) xq[d] = *(const f16x8*)(x1 + 32 * P7_RC(d));
;         bf16x8 b0hN = *(const bf16x8*)(WRH + (size_t)i * D_ + 32 * rot + 8 * g4), b1hN = *(const bf16x8*)(WRH + (size_t)(i + 16) * D_ + 32 * rot + 8 * g4), b0lN = *(const bf16x8*)(WRL + (size_t)i * D_ + 32 * rot + 8 * g4), b1lN = *(const bf16x8*)(WRL + (size_t)(i + 16) * D_ + 32 * rot + 8 * g4);
;         for (int c4 = 0; c4 < 64; c4 += 4) {
; #pragma unroll
;           for (int d = 0; d < 4; ++d) { const int cl = c4 + d, c = P7_RC(cl);
;             const f32x8 xf = __builtin_convertvector(xq[d], f32x8); const f32x4 xa = {xf[0], xf[1], xf[2], xf[3]}, xb = {xf[4], xf[5], xf[6], xf[7]}, ga = *(const f32x4*)(fg + 32 * c), gb = *(const f32x4*)(fg + 32 * c + 4);
.LBB0_896:
	s_mov_b64 s[0:1], exec
	v_readlane_b32 s2, v254, 28
	v_readlane_b32 s3, v254, 29
	s_and_b64 s[2:3], s[0:1], s[2:3]
	s_mov_b64 exec, s[2:3]
	ds_write_b32 v76, v43
	s_or_b64 exec, exec, s[0:1]
	s_lshl_b32 s0, s83, 7
	v_writelane_b32 v254, s0, 32
	v_add_u32_e32 v64, s0, v75
	v_ashrrev_i32_e32 v65, 31, v64
	v_readlane_b32 s0, v254, 34
	v_lshlrev_b64 v[2:3], 7, v[64:65]
	v_readlane_b32 s1, v254, 35
	s_waitcnt lgkmcnt(0)
	s_barrier
	v_lshl_add_u64 v[18:19], s[0:1], 0, v[2:3]
	global_load_dwordx4 v[66:69], v[18:19], off
	global_load_dwordx4 v[70:73], v[18:19], off offset:16
	global_load_dwordx4 v[84:87], v[18:19], off offset:32
	global_load_dwordx4 v[88:91], v[18:19], off offset:48
	global_load_dwordx4 v[92:95], v[18:19], off offset:64
	global_load_dwordx4 v[96:99], v[18:19], off offset:80
	global_load_dwordx4 v[100:103], v[18:19], off offset:96
	global_load_dwordx4 v[104:107], v[18:19], off offset:112
	flat_load_dwordx2 v[108:109], v[58:59] offset:160
	global_load_dwordx4 v[6:9], v[48:49], off
	global_load_dwordx4 v[2:5], v[50:51], off
	global_load_dwordx4 v[10:13], v[52:53], off
	global_load_dwordx4 v[14:17], v[54:55], off
	v_lshlrev_b64 v[18:19], 12, v[64:65]
	v_readlane_b32 s0, v254, 38
	v_lshl_add_u64 v[62:63], v[44:45], 0, v[18:19]
	v_readlane_b32 s1, v254, 39
	v_lshlrev_b64 v[64:65], 11, v[64:65]
	s_mov_b32 s6, 3
	v_lshl_add_u64 v[22:23], v[62:63], 0, s[0:1]
	v_readlane_b32 s0, v254, 40
	v_readlane_b32 s1, v254, 41
	v_readlane_b32 s7, v254, 36
	v_lshl_add_u64 v[64:65], v[46:47], 0, v[64:65]
	v_lshl_add_u64 v[24:25], v[62:63], 0, s[0:1]
	v_readlane_b32 s0, v254, 54
	v_readlane_b32 s1, v254, 55
	s_waitcnt vmcnt(0)
	v_mov_b32_e32 v110, v66
	v_lshl_add_u64 v[38:39], v[62:63], 0, s[0:1]
	v_readlane_b32 s0, v254, 56
	v_readlane_b32 s1, v254, 57
	v_mov_b32_e32 v111, v70
	v_mov_b32_e32 v70, v67
	v_lshl_add_u64 v[40:41], v[62:63], 0, s[0:1]
	global_load_dwordx4 v[34:37], v[22:23], off
	global_load_dwordx4 v[30:33], v[24:25], off
	global_load_dwordx4 v[26:29], v[38:39], off
	global_load_dwordx4 v[18:21], v[40:41], off
	v_mov_b32_e32 v66, v68
	v_mov_b32_e32 v67, v72
	v_mov_b32_e32 v72, v69
	v_mov_b32_e32 v68, v85
	v_mov_b32_e32 v69, v86
	v_mov_b32_e32 v85, v87
	v_pk_add_f32 v[70:71], v[110:111], v[70:71]
	v_pk_add_f32 v[66:67], v[66:67], v[72:73]
	v_pk_add_f32 v[68:69], v[68:69], v[84:85]
	v_pk_add_f32 v[66:67], v[70:71], v[66:67]
	v_pk_add_f32 v[68:69], v[68:69], v[68:69] op_sel:[0,1] op_sel_hi:[1,0]
	v_add_f32_e32 v41, 0, v66
	v_add_f32_e32 v86, v88, v89
	v_add_f32_e32 v88, v90, v91
	v_mov_b32_e32 v91, v92
	v_mov_b32_e32 v87, v94
	v_mov_b32_e32 v89, v95
	v_mov_b32_e32 v69, v93
	v_add_f32_e32 v90, v41, v67
	v_mov_b32_e32 v94, v97
	v_mov_b32_e32 v95, v98
	v_mov_b32_e32 v97, v99
	v_pk_add_f32 v[72:73], v[86:87], v[88:89]
	v_pk_add_f32 v[66:67], v[90:91], v[68:69]
	v_pk_add_f32 v[84:85], v[94:95], v[96:97]
	v_pk_add_f32 v[66:67], v[66:67], v[72:73]
	v_pk_add_f32 v[70:71], v[84:85], v[84:85] op_sel:[0,1] op_sel_hi:[1,0]
	v_pk_add_f32 v[66:67], v[66:67], v[66:67] op_sel:[0,1] op_sel_hi:[1,0]
	v_add_f32_e32 v98, v100, v101
	v_add_f32_e32 v100, v102, v103
	v_mov_b32_e32 v99, v106
	v_mov_b32_e32 v101, v107
	v_mov_b32_e32 v71, v105
	v_mov_b32_e32 v67, v104
	v_pk_add_f32 v[86:87], v[98:99], v[100:101]
	v_pk_add_f32 v[66:67], v[66:67], v[70:71]
	s_mov_b32 s0, 0x800000
	v_pk_add_f32 v[66:67], v[66:67], v[86:87]
	v_mov_b32_e32 v22, 0
	v_add_f32_e32 v41, v66, v67
	v_fmamk_f32 v41, v41, 0x3a000000, v78
	v_mul_f32_e32 v42, 0x4b800000, v41
	v_cmp_gt_f32_e32 vcc, s0, v41
	v_mov_b32_e32 v23, v22
	v_mov_b32_e32 v24, v22
	v_cndmask_b32_e32 v41, v41, v42, vcc
	v_rsq_f32_e32 v41, v41
	v_mov_b32_e32 v25, v22
	v_mov_b32_e32 v38, v22
	v_mov_b32_e32 v39, v22
	v_mul_f32_e32 v42, 0x45800000, v41
	v_mov_b32_e32 v40, v22
	s_waitcnt vmcnt(0) lgkmcnt(0)
	v_lshl_add_u64 v[66:67], v[108:109], 0, v[60:61]
	v_cndmask_b32_e32 v83, v41, v42, vcc
	v_mov_b32_e32 v41, v22
	v_readlane_b32 s0, v254, 4
	s_nop 0
	s_cmpk_lt_u32 s0, 0x100
	s_cbranch_scc1 .Lp7_nostag
	s_sleep 6
.Lp7_nostag:
.LBB0_899:
	s_add_i32 s0, s7, 0xffffffa0
	s_sub_i32 s3, s7, 64
	s_add_i32 s4, s6, -2
	s_add_i32 s10, s6, -1
	s_min_u32 s12, s6, 59
	s_and_b32 s90, s0, 0x7e0
	s_mov_b32 s13, s91
	s_and_b32 s14, s3, 0x7e0
	s_min_u32 s3, s4, 59
	s_min_u32 s4, s10, 59
	s_add_i32 s10, s12, s85
	s_lshl_b32 s12, s90, 2
	s_waitcnt vmcnt(5)
	v_cvt_f32_f16_sdwa v138, v27 dst_sel:DWORD dst_unused:UNUSED_PAD src0_sel:WORD_1
	v_cvt_f32_f16_sdwa v139, v26 dst_sel:DWORD dst_unused:UNUSED_PAD src0_sel:WORD_1
	v_cvt_f32_f16_e32 v142, v27
	v_cvt_f32_f16_e32 v143, v26
	s_waitcnt vmcnt(5)
; __device__ __forceinline__ void p7_ffn_prep(const Ctx& C, bool dummy = false) {
;     ...
;           for (int d = 0; d < 4; ++d) { const int cl = c4 + d, c = P7_RC(cl);
;             const f32x8 xf = __builtin_convertvector(xq[d], f32x8); const f32x4 xa = {xf[0], xf[1], xf[2], xf[3]}, xb = {xf[4], xf[5], xf[6], xf[7]}, ga = *(const f32x4*)(fg + 32 * c), gb = *(const f32x4*)(fg + 32 * c + 4);
;             const bf16x8 b0h = b0hN, b1h = b1hN, b0l = b0lN, b1l = b1lN;
;             { const int cx = P7_RC(cl + 4 < 64 ? cl + 4 : 63); xq[d] = *(const f16x8*)(x1 + 32 * cx);
;               const int cn = P7_RC(cl < 63 ? cl + 1 : cl); const size_t bn = (size_t)i * D_ + 32 * cn + 8 * g4;
;               b0hN = *(const bf16x8*)(WRH + bn); b1hN = *(const bf16x8*)(WRH + bn + (size_t)16 * D_); b0lN = *(const bf16x8*)(WRL + bn); b1lN = *(const bf16x8*)(WRL + bn + (size_t)16 * D_); }
;             float h[8]; h[0] = xa[0] * ga[0] * rstd; h[1] = xa[1] * ga[1] * rstd; h[2] = xa[2] * ga[2] * rstd; h[3] = xa[3] * ga[3] * rstd; h[4] = xb[0] * gb[0] * rstd; h[5] = xb[1] * gb[1] * rstd; h[6] = xb[2] * gb[2] * rstd; h[7] = xb[3] * gb[3] * rstd;
;             u32x4 hi; hi.x = cvt_pk_bf16(h[0], h[1]); hi.y = cvt_pk_bf16(h[2], h[3]); hi.z = cvt_pk_bf16(h[4], h[5]); hi.w = cvt_pk_bf16(h[6], h[7]);
;             { u32x2 w8; w8.x = pk4_fp8(h[0], h[1], h[2], h[3]); w8.y = pk4_fp8(h[4], h[5], h[6], h[7]); *(u32x2*)(h2 + 32 * c) = w8; }
;             u32x4 lo; lo.x = cvt_pk_bf16(h[0] - __uint_as_float(hi.x << 16), h[1] - __uint_as_float(hi.x & 0xFFFF0000u)); lo.y = cvt_pk_bf16(h[2] - __uint_as_float(hi.y << 16), h[3] - __uint_as_float(hi.y & 0xFFFF0000u));
;             lo.z = cvt_pk_bf16(h[4] - __uint_as_float(hi.z << 16), h[5] - __uint_as_float(hi.z & 0xFFFF0000u)); lo.w = cvt_pk_bf16(h[6] - __uint_as_float(hi.w << 16), h[7] - __uint_as_float(hi.w & 0xFFFF0000u));
;             const bf16x8 ah = __builtin_bit_cast(bf16x8, hi), al = __builtin_bit_cast(bf16x8, lo);
;             a0 = __builtin_amdgcn_mfma_f32_16x16x32_bf16(ah, b0h, a0, 0, 0, 0); a0 = __builtin_amdgcn_mfma_f32_16x16x32_bf16(ah, b0l, a0, 0, 0, 0); a0 = __builtin_amdgcn_mfma_f32_16x16x32_bf16(al, b0h, a0, 0, 0, 0);
;             a1 = __builtin_amdgcn_mfma_f32_16x16x32_bf16(ah, b1h, a1, 0, 0, 0); a1 = __builtin_amdgcn_mfma_f32_16x16x32_bf16(ah, b1l, a1, 0, 0, 0); a1 = __builtin_amdgcn_mfma_f32_16x16x32_bf16(al, b1h, a1, 0, 0, 0);
	v_cvt_f32_f16_sdwa v147, v18 dst_sel:DWORD dst_unused:UNUSED_PAD src0_sel:WORD_1
	v_cvt_f32_f16_e32 v151, v18
	v_or_b32_e32 v18, s14, v77
	v_lshl_add_u64 v[26:27], v[66:67], 0, s[12:13]
	v_cvt_f32_f16_sdwa v136, v29 dst_sel:DWORD dst_unused:UNUSED_PAD src0_sel:WORD_1
	v_cvt_f32_f16_sdwa v137, v28 dst_sel:DWORD dst_unused:UNUSED_PAD src0_sel:WORD_1
	v_cvt_f32_f16_e32 v140, v29
	v_cvt_f32_f16_e32 v141, v28
	v_cvt_f32_f16_sdwa v144, v21 dst_sel:DWORD dst_unused:UNUSED_PAD src0_sel:WORD_1
	v_cvt_f32_f16_sdwa v145, v20 dst_sel:DWORD dst_unused:UNUSED_PAD src0_sel:WORD_1
	v_cvt_f32_f16_sdwa v146, v19 dst_sel:DWORD dst_unused:UNUSED_PAD src0_sel:WORD_1
	v_cvt_f32_f16_e32 v148, v21
	v_cvt_f32_f16_e32 v149, v20
	v_cvt_f32_f16_e32 v150, v19
	v_lshlrev_b32_e32 v42, 1, v18
	global_load_dwordx4 v[18:21], v[26:27], off
	s_nop 0
	global_load_dwordx4 v[26:29], v[26:27], off offset:16
	s_add_i32 s3, s3, s85
	v_cvt_f32_f16_sdwa v130, v31 dst_sel:DWORD dst_unused:UNUSED_PAD src0_sel:WORD_1
	v_cvt_f32_f16_sdwa v131, v30 dst_sel:DWORD dst_unused:UNUSED_PAD src0_sel:WORD_1
	v_cvt_f32_f16_e32 v134, v31
	v_cvt_f32_f16_e32 v135, v30
	v_lshl_add_u64 v[30:31], v[64:65], 0, s[90:91]
	s_lshl_b32 s90, s14, 2
	s_lshl_b32 s3, s3, 6
	v_cvt_f32_f16_sdwa v122, v35 dst_sel:DWORD dst_unused:UNUSED_PAD src0_sel:WORD_1
	v_cvt_f32_f16_sdwa v123, v34 dst_sel:DWORD dst_unused:UNUSED_PAD src0_sel:WORD_1
	v_cvt_f32_f16_e32 v126, v35
	v_cvt_f32_f16_e32 v127, v34
	v_cvt_f32_f16_sdwa v128, v33 dst_sel:DWORD dst_unused:UNUSED_PAD src0_sel:WORD_1
	v_cvt_f32_f16_sdwa v129, v32 dst_sel:DWORD dst_unused:UNUSED_PAD src0_sel:WORD_1
	v_cvt_f32_f16_e32 v132, v33
	v_cvt_f32_f16_e32 v133, v32
	s_sub_i32 s9, s7, 32
	v_lshl_add_u64 v[32:33], v[66:67], 0, s[90:91]
	v_lshl_add_u64 v[34:35], s[86:87], 0, v[42:43]
	s_and_b32 s90, s3, 0xfc0
	v_add_co_u32_e32 v94, vcc, s33, v34
	v_lshl_add_u64 v[100:101], v[62:63], 0, s[90:91]
	s_and_b32 s90, s9, 0x7e0
	v_cvt_f32_f16_sdwa v106, v37 dst_sel:DWORD dst_unused:UNUSED_PAD src0_sel:WORD_1
	v_cvt_f32_f16_sdwa v107, v36 dst_sel:DWORD dst_unused:UNUSED_PAD src0_sel:WORD_1
	v_cvt_f32_f16_e32 v124, v37
	v_cvt_f32_f16_e32 v125, v36
	global_load_dwordx4 v[84:87], v42, s[86:87]
	global_load_dwordx4 v[88:91], v42, s[88:89]
	v_lshl_add_u64 v[36:37], s[88:89], 0, v[42:43]
	v_addc_co_u32_e32 v95, vcc, 0, v35, vcc
	v_or_b32_e32 v42, s90, v77
	v_add_co_u32_e32 v96, vcc, s33, v36
	v_lshlrev_b32_e32 v42, 1, v42
	s_add_i32 s8, s6, -3
	v_addc_co_u32_e32 v97, vcc, 0, v37, vcc
	v_lshl_add_u64 v[102:103], s[86:87], 0, v[42:43]
	s_min_u32 s0, s8, 59
	v_add_co_u32_e32 v102, vcc, s33, v102
	s_add_i32 s0, s0, s85
	v_lshl_add_u64 v[104:105], s[88:89], 0, v[42:43]
	v_addc_co_u32_e32 v103, vcc, 0, v103, vcc
	s_mov_b32 s15, s91
	s_lshl_b32 s0, s0, 6
	v_add_co_u32_e32 v120, vcc, s33, v104
	s_mov_b32 s11, s91
	v_lshl_add_u64 v[108:109], v[64:65], 0, s[14:15]
	s_lshl_b32 s14, s10, 6
	s_and_b32 s10, s0, 0xfc0
	v_addc_co_u32_e32 v121, vcc, 0, v105, vcc
	v_lshl_add_u64 v[92:93], v[62:63], 0, s[10:11]
	v_mov_b32_e32 v68, v43
	v_mov_b32_e32 v69, v43
	global_load_dwordx4 v[34:37], v[92:93], off
	s_nop 0
	global_load_dwordx4 v[92:95], v[94:95], off
	s_nop 0
	global_load_dwordx4 v[96:99], v[96:97], off
	s_and_b32 s2, s7, 0x7e0
	v_or_b32_e32 v152, s2, v77
	v_mov_b32_e32 v70, v43
	v_mov_b32_e32 v71, v43
	s_add_i32 s4, s4, s85
	s_mov_b32 s1, s91
	s_lshl_b32 s4, s4, 6
	s_lshl_b32 s0, s90, 2
	s_mov_b32 s5, s91
	s_and_b32 s4, s4, 0xfc0
	v_lshl_add_u64 v[114:115], v[66:67], 0, s[0:1]
	v_lshl_add_u64 v[110:111], v[62:63], 0, s[4:5]
	v_mov_b32_e32 v72, v43
	v_mov_b32_e32 v73, v43
	v_lshl_add_u64 v[112:113], v[64:65], 0, s[90:91]
	s_lshl_b32 s90, s2, 2
	s_waitcnt vmcnt(5) lgkmcnt(0)
	v_mul_f32_e32 v104, v18, v127
	v_mul_f32_e32 v105, v19, v123
	v_mul_f32_e32 v123, v20, v126
	v_mul_f32_e32 v122, v21, v122
	v_mul_f32_e32 v125, v125, v26
	v_mul_f32_e32 v107, v107, v27
	v_mul_f32_e32 v124, v124, v28
	v_mul_f32_e32 v106, v106, v29
	v_mul_f32_e32 v26, v83, v104
	v_mul_f32_e32 v27, v83, v105
	v_mul_f32_e32 v28, v83, v123
	v_mul_f32_e32 v29, v83, v122
	v_mul_f32_e32 v126, v83, v125
	v_mul_f32_e32 v127, v83, v107
	v_cvt_pk_bf16_f32 v18, v26, v27
	v_cvt_pk_bf16_f32 v19, v28, v29
	v_med3_f32 v26, v26, s82, v81
	v_med3_f32 v27, v27, s82, v81
	v_med3_f32 v156, v28, s82, v81
	v_med3_f32 v157, v29, s82, v81
	v_med3_f32 v28, v126, s82, v81
	v_med3_f32 v29, v127, s82, v81
	v_cvt_pk_fp8_f32 v68, v26, v27
	v_cvt_pk_fp8_f32 v69, v28, v29
	v_mul_f32_e32 v154, v83, v124
	v_mul_f32_e32 v155, v83, v106
	v_cvt_pk_bf16_f32 v20, v126, v127
	v_med3_f32 v126, v154, s82, v81
	v_med3_f32 v127, v155, s82, v81
	v_cvt_pk_bf16_f32 v21, v154, v155
	v_cvt_pk_fp8_f32 v68, v156, v157 op_sel:[0,0,1]
	v_mfma_f32_16x16x32_bf16 v[22:25], v[18:21], v[6:9], v[22:25]
	v_cvt_pk_fp8_f32 v69, v126, v127 op_sel:[0,0,1]
	v_lshlrev_b32_e32 v154, 16, v18
	v_and_b32_e32 v155, 0xffff0000, v18
	v_mfma_f32_16x16x32_bf16 v[26:29], v[18:21], v[2:5], v[38:41]
	v_lshlrev_b32_e32 v158, 16, v19
	v_and_b32_e32 v159, 0xffff0000, v19
	v_lshlrev_b32_e32 v160, 16, v20
	v_and_b32_e32 v161, 0xffff0000, v20
	v_lshlrev_b32_e32 v162, 16, v21
	v_and_b32_e32 v163, 0xffff0000, v21
	v_fma_f32 v38, v83, v104, -v154
	v_fma_f32 v39, v83, v105, -v155
	v_fma_f32 v40, v83, v123, -v158
	v_fma_f32 v41, v83, v122, -v159
	v_fma_f32 v104, v83, v125, -v160
	v_fma_f32 v105, v83, v107, -v161
	v_fma_f32 v107, v83, v124, -v162
	v_fma_f32 v106, v83, v106, -v163
	v_mfma_f32_16x16x32_bf16 v[10:13], v[18:21], v[10:13], v[22:25]
	global_store_dwordx2 v[30:31], v[68:69], off
	v_lshl_add_u64 v[116:117], v[66:67], 0, s[90:91]
	s_and_b32 s90, s14, 0xfc0
	v_mfma_f32_16x16x32_bf16 v[14:17], v[18:21], v[14:17], v[26:29]
	v_cvt_pk_bf16_f32 v18, v38, v39
	v_cvt_pk_bf16_f32 v19, v40, v41
	v_cvt_pk_bf16_f32 v20, v104, v105
	v_cvt_pk_bf16_f32 v21, v107, v106
	global_load_dwordx4 v[22:25], v[32:33], off
	s_nop 1
	global_load_dwordx4 v[26:29], v[32:33], off offset:16
	s_nop 0
	global_load_dwordx4 v[30:33], v[100:101], off
	global_load_dwordx4 v[38:41], v[102:103], off
	s_nop 0
	global_load_dwordx4 v[100:103], v42, s[88:89]
	v_mfma_f32_16x16x32_bf16 v[6:9], v[18:21], v[6:9], v[10:13]
	global_load_dwordx4 v[104:107], v42, s[86:87]
	s_nop 1
	global_load_dwordx4 v[10:13], v[120:121], off
	v_lshlrev_b32_e32 v42, 1, v152
	s_cmp_lt_u32 s6, 63
	v_mfma_f32_16x16x32_bf16 v[2:5], v[18:21], v[2:5], v[14:17]
	s_cselect_b64 s[0:1], -1, 0
	s_cmp_lg_u64 s[0:1], 0
	s_addc_u32 s0, s84, s6
	v_lshl_add_u64 v[14:15], s[86:87], 0, v[42:43]
	v_add_co_u32_e32 v68, vcc, s33, v14
	v_lshl_add_u64 v[16:17], s[88:89], 0, v[42:43]
	s_nop 0
	v_addc_co_u32_e32 v69, vcc, 0, v15, vcc
	v_add_co_u32_e32 v120, vcc, s33, v16
	s_lshl_b32 s0, s0, 5
	s_nop 0
	v_addc_co_u32_e32 v121, vcc, 0, v17, vcc
	s_and_b32 s0, s0, 0x7e0
	v_or_b32_e32 v153, s0, v77
	v_lshl_add_u64 v[118:119], v[62:63], 0, s[90:91]
	s_mov_b32 s3, s91
	s_add_i32 s6, s6, 4
	s_addk_i32 s7, 0x80
	s_cmp_gt_u32 s8, 59
	s_waitcnt vmcnt(5) lgkmcnt(0)
; __device__ __forceinline__ void p7_ffn_prep(const Ctx& C, bool dummy = false) {
;     ...
;           for (int d = 0; d < 4; ++d) { const int cl = c4 + d, c = P7_RC(cl);
;             const f32x8 xf = __builtin_convertvector(xq[d], f32x8); const f32x4 xa = {xf[0], xf[1], xf[2], xf[3]}, xb = {xf[4], xf[5], xf[6], xf[7]}, ga = *(const f32x4*)(fg + 32 * c), gb = *(const f32x4*)(fg + 32 * c + 4);
;             const bf16x8 b0h = b0hN, b1h = b1hN, b0l = b0lN, b1l = b1lN;
;             { const int cx = P7_RC(cl + 4 < 64 ? cl + 4 : 63); xq[d] = *(const f16x8*)(x1 + 32 * cx);
;               const int cn = P7_RC(cl < 63 ? cl + 1 : cl); const size_t bn = (size_t)i * D_ + 32 * cn + 8 * g4;
;               b0hN = *(const bf16x8*)(WRH + bn); b1hN = *(const bf16x8*)(WRH + bn + (size_t)16 * D_); b0lN = *(const bf16x8*)(WRL + bn); b1lN = *(const bf16x8*)(WRL + bn + (size_t)16 * D_); }
;             float h[8]; h[0] = xa[0] * ga[0] * rstd; h[1] = xa[1] * ga[1] * rstd; h[2] = xa[2] * ga[2] * rstd; h[3] = xa[3] * ga[3] * rstd; h[4] = xb[0] * gb[0] * rstd; h[5] = xb[1] * gb[1] * rstd; h[6] = xb[2] * gb[2] * rstd; h[7] = xb[3] * gb[3] * rstd;
;             u32x4 hi; hi.x = cvt_pk_bf16(h[0], h[1]); hi.y = cvt_pk_bf16(h[2], h[3]); hi.z = cvt_pk_bf16(h[4], h[5]); hi.w = cvt_pk_bf16(h[6], h[7]);
;             { u32x2 w8; w8.x = pk4_fp8(h[0], h[1], h[2], h[3]); w8.y = pk4_fp8(h[4], h[5], h[6], h[7]); *(u32x2*)(h2 + 32 * c) = w8; }
;             u32x4 lo; lo.x = cvt_pk_bf16(h[0] - __uint_as_float(hi.x << 16), h[1] - __uint_as_float(hi.x & 0xFFFF0000u)); lo.y = cvt_pk_bf16(h[2] - __uint_as_float(hi.y << 16), h[3] - __uint_as_float(hi.y & 0xFFFF0000u));
;             lo.z = cvt_pk_bf16(h[4] - __uint_as_float(hi.z << 16), h[5] - __uint_as_float(hi.z & 0xFFFF0000u)); lo.w = cvt_pk_bf16(h[6] - __uint_as_float(hi.w << 16), h[7] - __uint_as_float(hi.w & 0xFFFF0000u));
;             const bf16x8 ah = __builtin_bit_cast(bf16x8, hi), al = __builtin_bit_cast(bf16x8, lo);
;             a0 = __builtin_amdgcn_mfma_f32_16x16x32_bf16(ah, b0h, a0, 0, 0, 0); a0 = __builtin_amdgcn_mfma_f32_16x16x32_bf16(ah, b0l, a0, 0, 0, 0); a0 = __builtin_amdgcn_mfma_f32_16x16x32_bf16(al, b0h, a0, 0, 0, 0);
;             a1 = __builtin_amdgcn_mfma_f32_16x16x32_bf16(ah, b1h, a1, 0, 0, 0); a1 = __builtin_amdgcn_mfma_f32_16x16x32_bf16(ah, b1l, a1, 0, 0, 0); a1 = __builtin_amdgcn_mfma_f32_16x16x32_bf16(al, b1h, a1, 0, 0, 0);
	v_mul_f32_e32 v18, v135, v22
	v_mul_f32_e32 v19, v131, v23
	v_mul_f32_e32 v22, v133, v26
	v_mul_f32_e32 v23, v129, v27
	v_mul_f32_e32 v20, v134, v24
	v_mul_f32_e32 v21, v130, v25
	v_mul_f32_e32 v26, v83, v18
	v_mul_f32_e32 v27, v83, v19
	v_mul_f32_e32 v122, v83, v22
	v_mul_f32_e32 v123, v83, v23
	v_mul_f32_e32 v24, v132, v28
	v_mul_f32_e32 v25, v128, v29
	v_mul_f32_e32 v28, v83, v20
	v_mul_f32_e32 v29, v83, v21
	v_cvt_pk_bf16_f32 v14, v26, v27
	v_cvt_pk_bf16_f32 v15, v28, v29
	v_cvt_pk_bf16_f32 v16, v122, v123
	v_med3_f32 v26, v26, s82, v81
	v_med3_f32 v27, v27, s82, v81
	v_med3_f32 v122, v122, s82, v81
	v_med3_f32 v123, v123, s82, v81
	v_cvt_pk_fp8_f32 v70, v26, v27
	v_cvt_pk_fp8_f32 v71, v122, v123
	v_mul_f32_e32 v124, v83, v24
	v_mul_f32_e32 v125, v83, v25
	v_cvt_pk_bf16_f32 v17, v124, v125
	v_med3_f32 v28, v28, s82, v81
	v_med3_f32 v29, v29, s82, v81
	v_med3_f32 v124, v124, s82, v81
	v_med3_f32 v125, v125, s82, v81
	v_mfma_f32_16x16x32_bf16 v[6:9], v[14:17], v[84:87], v[6:9]
	v_cvt_pk_fp8_f32 v70, v28, v29 op_sel:[0,0,1]
	v_cvt_pk_fp8_f32 v71, v124, v125 op_sel:[0,0,1]
	v_lshlrev_b32_e32 v26, 16, v14
	v_mfma_f32_16x16x32_bf16 v[2:5], v[14:17], v[92:95], v[2:5]
	v_and_b32_e32 v27, 0xffff0000, v14
	v_lshlrev_b32_e32 v122, 16, v15
	v_and_b32_e32 v123, 0xffff0000, v15
	v_lshlrev_b32_e32 v126, 16, v16
	v_and_b32_e32 v127, 0xffff0000, v16
	v_lshlrev_b32_e32 v128, 16, v17
	v_and_b32_e32 v129, 0xffff0000, v17
	v_fma_f32 v18, v83, v18, -v26
	v_fma_f32 v19, v83, v19, -v27
	v_fma_f32 v20, v83, v20, -v122
	v_fma_f32 v21, v83, v21, -v123
	v_fma_f32 v22, v83, v22, -v126
	v_fma_f32 v23, v83, v23, -v127
	v_fma_f32 v24, v83, v24, -v128
	v_fma_f32 v25, v83, v25, -v129
	v_mfma_f32_16x16x32_bf16 v[6:9], v[14:17], v[88:91], v[6:9]
	global_store_dwordx2 v[108:109], v[70:71], off
	v_mfma_f32_16x16x32_bf16 v[2:5], v[14:17], v[96:99], v[2:5]
	v_cvt_pk_bf16_f32 v14, v18, v19
	v_cvt_pk_bf16_f32 v15, v20, v21
	v_cvt_pk_bf16_f32 v16, v22, v23
	v_cvt_pk_bf16_f32 v17, v24, v25
	global_load_dwordx4 v[18:21], v[114:115], off
	global_load_dwordx4 v[22:25], v[114:115], off offset:16
	global_load_dwordx4 v[26:29], v[110:111], off
	s_nop 0
	global_load_dwordx4 v[68:71], v[68:69], off
	s_nop 0
	global_load_dwordx4 v[88:91], v42, s[88:89]
	v_mfma_f32_16x16x32_bf16 v[2:5], v[14:17], v[92:95], v[2:5]
	s_waitcnt vmcnt(3) lgkmcnt(0)
	v_mul_f32_e32 v18, v143, v18
	v_mul_f32_e32 v19, v139, v19
	v_mul_f32_e32 v22, v141, v22
	v_mul_f32_e32 v23, v137, v23
	v_mul_f32_e32 v20, v142, v20
	v_mul_f32_e32 v21, v138, v21
	v_mul_f32_e32 v92, v83, v18
	v_mul_f32_e32 v93, v83, v19
	v_mul_f32_e32 v108, v83, v22
	v_mul_f32_e32 v109, v83, v23
	v_mfma_f32_16x16x32_bf16 v[6:9], v[14:17], v[84:87], v[6:9]
	global_load_dwordx4 v[84:87], v42, s[86:87]
	global_load_dwordx4 v[96:99], v[120:121], off
	v_mul_f32_e32 v94, v83, v20
	v_mul_f32_e32 v95, v83, v21
	v_cvt_pk_bf16_f32 v14, v92, v93
	v_cvt_pk_bf16_f32 v15, v94, v95
	v_cvt_pk_bf16_f32 v16, v108, v109
	v_med3_f32 v92, v92, s82, v81
	v_med3_f32 v93, v93, s82, v81
	v_med3_f32 v108, v108, s82, v81
	v_med3_f32 v109, v109, s82, v81
	v_cvt_pk_fp8_f32 v72, v92, v93
	v_cvt_pk_fp8_f32 v73, v108, v109
	v_mul_f32_e32 v24, v140, v24
	v_mul_f32_e32 v25, v136, v25
	v_mul_f32_e32 v110, v83, v24
	v_mul_f32_e32 v111, v83, v25
	v_cvt_pk_bf16_f32 v17, v110, v111
	v_med3_f32 v94, v94, s82, v81
	v_med3_f32 v95, v95, s82, v81
	v_med3_f32 v110, v110, s82, v81
	v_med3_f32 v111, v111, s82, v81
	v_cvt_pk_fp8_f32 v72, v94, v95 op_sel:[0,0,1]
	v_cvt_pk_fp8_f32 v73, v110, v111 op_sel:[0,0,1]
	v_lshlrev_b32_e32 v92, 16, v14
	v_and_b32_e32 v93, 0xffff0000, v14
	v_lshlrev_b32_e32 v108, 16, v15
	v_lshlrev_b32_e32 v122, 16, v16
	v_and_b32_e32 v123, 0xffff0000, v16
	v_lshlrev_b32_e32 v124, 16, v17
	v_and_b32_e32 v125, 0xffff0000, v17
	v_and_b32_e32 v109, 0xffff0000, v15
	v_fma_f32 v18, v83, v18, -v92
	v_fma_f32 v19, v83, v19, -v93
	v_fma_f32 v20, v83, v20, -v108
	v_fma_f32 v92, v83, v22, -v122
	v_fma_f32 v93, v83, v23, -v123
	v_fma_f32 v108, v83, v24, -v124
	v_fma_f32 v25, v83, v25, -v125
	v_fma_f32 v21, v83, v21, -v109
	global_store_dwordx2 v[112:113], v[72:73], off
	v_cvt_pk_bf16_f32 v22, v18, v19
	v_cvt_pk_bf16_f32 v23, v20, v21
	v_cvt_pk_bf16_f32 v24, v92, v93
	v_cvt_pk_bf16_f32 v25, v108, v25
	global_load_dwordx4 v[92:95], v[116:117], off
	global_load_dwordx4 v[108:111], v[116:117], off offset:16
	v_lshlrev_b32_e32 v42, 1, v153
	v_lshl_add_u64 v[114:115], s[86:87], 0, v[42:43]
	v_mfma_f32_16x16x32_bf16 v[6:9], v[14:17], v[104:107], v[6:9]
	v_add_co_u32_e32 v72, vcc, s33, v114
	v_lshl_add_u64 v[120:121], s[88:89], 0, v[42:43]
	v_mfma_f32_16x16x32_bf16 v[2:5], v[14:17], v[38:41], v[2:5]
	v_addc_co_u32_e32 v73, vcc, 0, v115, vcc
	v_add_co_u32_e32 v116, vcc, s33, v120
	v_mfma_f32_16x16x32_bf16 v[100:103], v[14:17], v[100:103], v[6:9]
	s_nop 0
	v_addc_co_u32_e32 v117, vcc, 0, v121, vcc
	s_waitcnt vmcnt(0) lgkmcnt(0)
; __device__ __forceinline__ void p7_ffn_prep(const Ctx& C, bool dummy = false) {
;     ...
;           for (int d = 0; d < 4; ++d) { const int cl = c4 + d, c = P7_RC(cl);
;             const f32x8 xf = __builtin_convertvector(xq[d], f32x8); const f32x4 xa = {xf[0], xf[1], xf[2], xf[3]}, xb = {xf[4], xf[5], xf[6], xf[7]}, ga = *(const f32x4*)(fg + 32 * c), gb = *(const f32x4*)(fg + 32 * c + 4);
;             const bf16x8 b0h = b0hN, b1h = b1hN, b0l = b0lN, b1l = b1lN;
;             { const int cx = P7_RC(cl + 4 < 64 ? cl + 4 : 63); xq[d] = *(const f16x8*)(x1 + 32 * cx);
;               const int cn = P7_RC(cl < 63 ? cl + 1 : cl); const size_t bn = (size_t)i * D_ + 32 * cn + 8 * g4;
;               b0hN = *(const bf16x8*)(WRH + bn); b1hN = *(const bf16x8*)(WRH + bn + (size_t)16 * D_); b0lN = *(const bf16x8*)(WRL + bn); b1lN = *(const bf16x8*)(WRL + bn + (size_t)16 * D_); }
;             float h[8]; h[0] = xa[0] * ga[0] * rstd; h[1] = xa[1] * ga[1] * rstd; h[2] = xa[2] * ga[2] * rstd; h[3] = xa[3] * ga[3] * rstd; h[4] = xb[0] * gb[0] * rstd; h[5] = xb[1] * gb[1] * rstd; h[6] = xb[2] * gb[2] * rstd; h[7] = xb[3] * gb[3] * rstd;
;             u32x4 hi; hi.x = cvt_pk_bf16(h[0], h[1]); hi.y = cvt_pk_bf16(h[2], h[3]); hi.z = cvt_pk_bf16(h[4], h[5]); hi.w = cvt_pk_bf16(h[6], h[7]);
;             { u32x2 w8; w8.x = pk4_fp8(h[0], h[1], h[2], h[3]); w8.y = pk4_fp8(h[4], h[5], h[6], h[7]); *(u32x2*)(h2 + 32 * c) = w8; }
;             u32x4 lo; lo.x = cvt_pk_bf16(h[0] - __uint_as_float(hi.x << 16), h[1] - __uint_as_float(hi.x & 0xFFFF0000u)); lo.y = cvt_pk_bf16(h[2] - __uint_as_float(hi.y << 16), h[3] - __uint_as_float(hi.y & 0xFFFF0000u));
;             lo.z = cvt_pk_bf16(h[4] - __uint_as_float(hi.z << 16), h[5] - __uint_as_float(hi.z & 0xFFFF0000u)); lo.w = cvt_pk_bf16(h[6] - __uint_as_float(hi.w << 16), h[7] - __uint_as_float(hi.w & 0xFFFF0000u));
;             const bf16x8 ah = __builtin_bit_cast(bf16x8, hi), al = __builtin_bit_cast(bf16x8, lo);
;             a0 = __builtin_amdgcn_mfma_f32_16x16x32_bf16(ah, b0h, a0, 0, 0, 0); a0 = __builtin_amdgcn_mfma_f32_16x16x32_bf16(ah, b0l, a0, 0, 0, 0); a0 = __builtin_amdgcn_mfma_f32_16x16x32_bf16(al, b0h, a0, 0, 0, 0);
;             a1 = __builtin_amdgcn_mfma_f32_16x16x32_bf16(ah, b1h, a1, 0, 0, 0); a1 = __builtin_amdgcn_mfma_f32_16x16x32_bf16(ah, b1l, a1, 0, 0, 0); a1 = __builtin_amdgcn_mfma_f32_16x16x32_bf16(al, b1h, a1, 0, 0, 0);
	v_mul_f32_e32 v108, v149, v108
	v_mfma_f32_16x16x32_bf16 v[112:115], v[14:17], v[10:13], v[2:5]
	global_load_dwordx4 v[18:21], v[118:119], off
	s_nop 1
	global_load_dwordx4 v[2:5], v[72:73], off
	global_load_dwordx4 v[10:13], v42, s[88:89]
	global_load_dwordx4 v[6:9], v42, s[86:87]
	global_load_dwordx4 v[14:17], v[116:117], off
	v_mul_f32_e32 v42, v151, v92
	v_mul_f32_e32 v109, v145, v109
	v_mfma_f32_16x16x32_bf16 v[100:103], v[22:25], v[104:107], v[100:103]
	v_mul_f32_e32 v106, v147, v93
	v_mul_f32_e32 v107, v150, v94
	v_mul_f32_e32 v92, v83, v42
	v_mfma_f32_16x16x32_bf16 v[22:25], v[22:25], v[38:41], v[112:115]
	v_mul_f32_e32 v93, v83, v106
	v_mul_f32_e32 v94, v83, v107
	v_mov_b32_e32 v72, v43
	v_mul_f32_e32 v112, v146, v95
	v_mul_f32_e32 v95, v83, v112
	v_mul_f32_e32 v113, v83, v108
	v_mul_f32_e32 v114, v83, v109
	v_mov_b32_e32 v73, v43
	v_mul_f32_e32 v110, v148, v110
	v_mul_f32_e32 v111, v144, v111
	v_cvt_pk_bf16_f32 v38, v92, v93
	v_cvt_pk_bf16_f32 v39, v94, v95
	v_med3_f32 v92, v92, s82, v81
	v_med3_f32 v93, v93, s82, v81
	v_med3_f32 v117, v94, s82, v81
	v_med3_f32 v118, v95, s82, v81
	v_med3_f32 v94, v113, s82, v81
	v_med3_f32 v95, v114, s82, v81
	v_mul_f32_e32 v115, v83, v110
	v_mul_f32_e32 v116, v83, v111
	v_cvt_pk_bf16_f32 v40, v113, v114
	v_cvt_pk_bf16_f32 v41, v115, v116
	v_cvt_pk_fp8_f32 v72, v92, v93
	v_cvt_pk_fp8_f32 v73, v94, v95
	v_mfma_f32_16x16x32_bf16 v[92:95], v[38:41], v[84:87], v[100:103]
	v_med3_f32 v113, v115, s82, v81
	v_med3_f32 v114, v116, s82, v81
	v_lshlrev_b32_e32 v115, 16, v38
	v_mfma_f32_16x16x32_bf16 v[22:25], v[38:41], v[68:71], v[22:25]
	v_and_b32_e32 v116, 0xffff0000, v38
	v_lshlrev_b32_e32 v119, 16, v39
	v_and_b32_e32 v120, 0xffff0000, v39
	v_lshlrev_b32_e32 v121, 16, v40
	v_and_b32_e32 v100, 0xffff0000, v40
	v_lshlrev_b32_e32 v101, 16, v41
	v_and_b32_e32 v102, 0xffff0000, v41
	v_cvt_pk_fp8_f32 v72, v117, v118 op_sel:[0,0,1]
	v_mfma_f32_16x16x32_bf16 v[88:91], v[38:41], v[88:91], v[92:95]
	v_cvt_pk_fp8_f32 v73, v113, v114 op_sel:[0,0,1]
	v_lshl_add_u64 v[104:105], v[64:65], 0, s[2:3]
	v_fma_f32 v42, v83, v42, -v115
	v_mfma_f32_16x16x32_bf16 v[38:41], v[38:41], v[96:99], v[22:25]
	v_fma_f32 v103, v83, v106, -v116
	v_fma_f32 v106, v83, v107, -v119
	v_fma_f32 v107, v83, v112, -v120
	v_fma_f32 v108, v83, v108, -v121
	v_fma_f32 v100, v83, v109, -v100
	v_fma_f32 v101, v83, v110, -v101
	v_fma_f32 v102, v83, v111, -v102
	global_store_dwordx2 v[104:105], v[72:73], off
	v_cvt_pk_bf16_f32 v92, v42, v103
	v_cvt_pk_bf16_f32 v93, v106, v107
	v_cvt_pk_bf16_f32 v94, v108, v100
	v_cvt_pk_bf16_f32 v95, v101, v102
	s_nop 0
	v_mfma_f32_16x16x32_bf16 v[22:25], v[92:95], v[84:87], v[88:91]
	v_mfma_f32_16x16x32_bf16 v[38:41], v[92:95], v[68:71], v[38:41]
	s_cbranch_scc0 .LBB0_899
	s_waitcnt vmcnt(4)
	v_add_u32_e32 v2, 0x400, v74
	s_nop 4
	ds_write2_b32 v2, v22, v38 offset1:16
	ds_write2_b32 v2, v23, v39 offset0:33 offset1:49
	ds_write2_b32 v2, v24, v40 offset0:66 offset1:82
	ds_write2_b32 v2, v25, v41 offset0:99 offset1:115
	s_waitcnt vmcnt(3)
	v_mov_b32_e32 v12, 0
	v_mov_b32_e32 v20, 0
	v_mov_b32_e32 v18, 0
	s_waitcnt vmcnt(1)
	v_mov_b32_e32 v16, 0
	v_mov_b32_e32 v14, 0
	v_mov_b32_e32 v10, 0
	v_mov_b32_e32 v11, 0
	v_mov_b32_e32 v13, 0
	v_mov_b32_e32 v2, 0
	v_mov_b32_e32 v4, 0
	v_mov_b32_e32 v6, 0
	v_mov_b32_e32 v8, 0
	s_mov_b64 s[2:3], exec
	v_readlane_b32 s0, v254, 22
	v_readlane_b32 s1, v254, 23
	v_writelane_b32 v254, s2, 30
	s_and_b64 s[0:1], s[2:3], s[0:1]
	s_nop 0
	v_writelane_b32 v254, s3, 31
	s_mov_b64 exec, s[0:1]
	s_cbranch_execz .LBB0_902
	v_readlane_b32 s0, v254, 15
	v_readlane_b32 s1, v254, 16
	v_add_u32_e32 v4, 0x400, v79
	ds_read2_b32 v[8:9], v4 offset1:1
	v_mov_b64_e32 v[2:3], s[0:1]
	flat_load_dwordx2 v[2:3], v[2:3] offset:176
	s_mov_b32 s0, 0xff800000
	s_waitcnt vmcnt(0) lgkmcnt(0)
	flat_load_dwordx4 v[4:7], v[2:3]
	flat_load_dwordx4 v[16:19], v[2:3] offset:16
	flat_load_dwordx4 v[20:23], v[2:3] offset:32
	flat_load_dwordx4 v[24:27], v[2:3] offset:48
	flat_load_dwordx4 v[28:31], v[2:3] offset:64
	flat_load_dwordx4 v[32:35], v[2:3] offset:80
	s_waitcnt vmcnt(0) lgkmcnt(0)
	v_add_f32_e32 v11, v8, v4
	v_add_u32_e32 v4, 0x408, v79
	v_add_f32_e32 v9, v9, v5
	ds_read2_b32 v[4:5], v4 offset1:1
	v_cmp_lg_f32_e32 vcc, s0, v11
	v_cmp_nlg_f32_e64 s[10:11], s0, v11
	s_waitcnt lgkmcnt(0)
	v_add_f32_e32 v8, v4, v6
	v_add_u32_e32 v4, 0x410, v79
	v_add_f32_e32 v7, v5, v7
	ds_read2_b32 v[4:5], v4 offset1:1
	s_waitcnt lgkmcnt(0)
	v_add_f32_e32 v15, v4, v16
	v_add_u32_e32 v4, 0x418, v79
	v_add_f32_e32 v13, v5, v17
	ds_read2_b32 v[4:5], v4 offset1:1
	s_waitcnt lgkmcnt(0)
	v_add_f32_e32 v12, v4, v18
	v_add_u32_e32 v4, 0x420, v79
	v_add_f32_e32 v10, v5, v19
	ds_read2_b32 v[4:5], v4 offset1:1
	s_waitcnt lgkmcnt(0)
	v_add_f32_e32 v19, v4, v20
	v_add_u32_e32 v4, 0x428, v79
	v_add_f32_e32 v17, v5, v21
	ds_read2_b32 v[4:5], v4 offset1:1
	s_waitcnt lgkmcnt(0)
	v_add_f32_e32 v16, v4, v22
	v_add_u32_e32 v4, 0x430, v79
	v_add_f32_e32 v14, v5, v23
	ds_read2_b32 v[4:5], v4 offset1:1
	s_waitcnt lgkmcnt(0)
	v_add_f32_e32 v23, v4, v24
	v_add_u32_e32 v4, 0x438, v79
	v_add_f32_e32 v21, v5, v25
	ds_read2_b32 v[4:5], v4 offset1:1
	s_waitcnt lgkmcnt(0)
	v_add_f32_e32 v20, v4, v26
	v_add_u32_e32 v4, 0x440, v79
	v_add_f32_e32 v18, v5, v27
	ds_read2_b32 v[4:5], v4 offset1:1
	s_waitcnt lgkmcnt(0)
	v_add_f32_e32 v27, v4, v28
	v_add_u32_e32 v4, 0x448, v79
	v_add_f32_e32 v25, v5, v29
	ds_read2_b32 v[4:5], v4 offset1:1
	s_waitcnt lgkmcnt(0)
	v_add_f32_e32 v24, v4, v30
	v_add_u32_e32 v4, 0x450, v79
	v_add_f32_e32 v22, v5, v31
	ds_read2_b32 v[4:5], v4 offset1:1
	s_waitcnt lgkmcnt(0)
; __device__ __forceinline__ void p7_ffn_prep(const Ctx& C, bool dummy = false) {
;     ...
;         if (lane < 16) {
;             float v[32];
; #pragma unroll
;             for (int e = 0; e < 32; ++e) v[e] = lg[lane * 33 + e] + C.ka->in[I_BR][e];
;             float tv[4];
; #pragma unroll
;             for (int k = 0; k < 4; ++k) { float best = -__builtin_inff(); int be = 0;
; #pragma unroll
;                 for (int e = 0; e < 32; ++e) { const bool taken = (k > 0 && e == e4[0]) || (k > 1 && e == e4[1]) || (k > 2 && e == e4[2]); if (!taken && v[e] > best) { best = v[e]; be = e; } }
;                 e4[k] = be; tv[k] = best; }
	v_add_f32_e32 v31, v4, v32
	v_add_u32_e32 v4, 0x458, v79
	v_add_f32_e32 v29, v5, v33
	ds_read2_b32 v[4:5], v4 offset1:1
	s_waitcnt lgkmcnt(0)
	v_add_f32_e32 v28, v4, v34
	v_add_f32_e32 v26, v5, v35
	flat_load_dwordx4 v[34:37], v[2:3] offset:96
	v_add_u32_e32 v4, 0x460, v79
	ds_read2_b32 v[4:5], v4 offset1:1
	s_waitcnt vmcnt(0) lgkmcnt(0)
	v_add_f32_e32 v34, v4, v34
	v_add_u32_e32 v4, 0x468, v79
	v_add_f32_e32 v33, v5, v35
	ds_read2_b32 v[4:5], v4 offset1:1
	s_waitcnt lgkmcnt(0)
	v_add_f32_e32 v32, v4, v36
	v_add_u32_e32 v4, 0x470, v79
	v_add_f32_e32 v30, v5, v37
	ds_read2_b32 v[36:37], v4 offset1:1
	flat_load_dwordx4 v[2:5], v[2:3] offset:112
	s_waitcnt vmcnt(0) lgkmcnt(0)
	v_add_f32_e32 v35, v36, v2
	v_add_u32_e32 v2, 0x478, v79
	v_add_f32_e32 v3, v37, v3
	ds_read2_b32 v[36:37], v2 offset1:1
	v_cndmask_b32_e32 v2, v82, v11, vcc
	v_cmp_gt_f32_e32 vcc, v9, v2
	s_waitcnt lgkmcnt(0)
	v_add_f32_e32 v36, v36, v4
	v_cndmask_b32_e32 v2, v2, v9, vcc
	v_cndmask_b32_e64 v4, 0, 1, vcc
	v_cmp_gt_f32_e32 vcc, v8, v2
	v_add_f32_e32 v5, v37, v5
	s_nop 0
	v_cndmask_b32_e32 v2, v2, v8, vcc
	v_cndmask_b32_e64 v4, v4, 2, vcc
	v_cmp_gt_f32_e32 vcc, v7, v2
	s_nop 1
	v_cndmask_b32_e32 v2, v2, v7, vcc
	v_cndmask_b32_e64 v4, v4, 3, vcc
	v_cmp_gt_f32_e32 vcc, v15, v2
	s_nop 1
	v_cndmask_b32_e32 v2, v2, v15, vcc
	v_cndmask_b32_e64 v4, v4, 4, vcc
	v_cmp_gt_f32_e32 vcc, v13, v2
	s_nop 1
	v_cndmask_b32_e32 v2, v2, v13, vcc
	v_cndmask_b32_e64 v4, v4, 5, vcc
	v_cmp_gt_f32_e32 vcc, v12, v2
	s_nop 1
	v_cndmask_b32_e32 v2, v2, v12, vcc
	v_cndmask_b32_e64 v4, v4, 6, vcc
	v_cmp_gt_f32_e32 vcc, v10, v2
	s_nop 1
	v_cndmask_b32_e32 v2, v2, v10, vcc
	v_cndmask_b32_e64 v4, v4, 7, vcc
	v_cmp_gt_f32_e32 vcc, v19, v2
	s_nop 1
	v_cndmask_b32_e32 v2, v2, v19, vcc
	v_cndmask_b32_e64 v4, v4, 8, vcc
	v_cmp_gt_f32_e32 vcc, v17, v2
	s_nop 1
	v_cndmask_b32_e32 v2, v2, v17, vcc
	v_cndmask_b32_e64 v4, v4, 9, vcc
	v_cmp_gt_f32_e32 vcc, v16, v2
	s_nop 1
	v_cndmask_b32_e32 v2, v2, v16, vcc
	v_cndmask_b32_e64 v4, v4, 10, vcc
	v_cmp_gt_f32_e32 vcc, v14, v2
	s_nop 1
	v_cndmask_b32_e32 v2, v2, v14, vcc
	v_cndmask_b32_e64 v4, v4, 11, vcc
	v_cmp_gt_f32_e32 vcc, v23, v2
	s_nop 1
	v_cndmask_b32_e32 v2, v2, v23, vcc
	v_cndmask_b32_e64 v4, v4, 12, vcc
	v_cmp_gt_f32_e32 vcc, v21, v2
	s_nop 1
	v_cndmask_b32_e32 v2, v2, v21, vcc
	v_cndmask_b32_e64 v4, v4, 13, vcc
	v_cmp_gt_f32_e32 vcc, v20, v2
	s_nop 1
	v_cndmask_b32_e32 v2, v2, v20, vcc
	v_cndmask_b32_e64 v4, v4, 14, vcc
	v_cmp_gt_f32_e32 vcc, v18, v2
	s_nop 1
	v_cndmask_b32_e32 v2, v2, v18, vcc
	v_cndmask_b32_e64 v4, v4, 15, vcc
	v_cmp_gt_f32_e32 vcc, v27, v2
	s_nop 1
	v_cndmask_b32_e32 v2, v2, v27, vcc
	v_cndmask_b32_e64 v4, v4, 16, vcc
	v_cmp_gt_f32_e32 vcc, v25, v2
	s_nop 1
	v_cndmask_b32_e32 v2, v2, v25, vcc
	v_cndmask_b32_e64 v4, v4, 17, vcc
	v_cmp_gt_f32_e32 vcc, v24, v2
	s_nop 1
	v_cndmask_b32_e32 v2, v2, v24, vcc
	v_cndmask_b32_e64 v4, v4, 18, vcc
	v_cmp_gt_f32_e32 vcc, v22, v2
	s_nop 1
	v_cndmask_b32_e32 v2, v2, v22, vcc
	v_cndmask_b32_e64 v4, v4, 19, vcc
	v_cmp_gt_f32_e32 vcc, v31, v2
	s_nop 1
	v_cndmask_b32_e32 v2, v2, v31, vcc
	v_cndmask_b32_e64 v4, v4, 20, vcc
	v_cmp_gt_f32_e32 vcc, v29, v2
	s_nop 1
	v_cndmask_b32_e32 v2, v2, v29, vcc
	v_cndmask_b32_e64 v4, v4, 21, vcc
	v_cmp_gt_f32_e32 vcc, v28, v2
	s_nop 1
	v_cndmask_b32_e32 v2, v2, v28, vcc
	v_cndmask_b32_e64 v4, v4, 22, vcc
	v_cmp_gt_f32_e32 vcc, v26, v2
	s_nop 1
	v_cndmask_b32_e32 v2, v2, v26, vcc
	v_cndmask_b32_e64 v4, v4, 23, vcc
	v_cmp_gt_f32_e32 vcc, v34, v2
	s_nop 1
	v_cndmask_b32_e32 v2, v2, v34, vcc
	v_cndmask_b32_e64 v4, v4, 24, vcc
	v_cmp_gt_f32_e32 vcc, v33, v2
	s_nop 1
	v_cndmask_b32_e32 v2, v2, v33, vcc
	v_cndmask_b32_e64 v4, v4, 25, vcc
	v_cmp_gt_f32_e32 vcc, v32, v2
	s_nop 1
	v_cndmask_b32_e32 v2, v2, v32, vcc
	v_cndmask_b32_e64 v4, v4, 26, vcc
	v_cmp_gt_f32_e32 vcc, v30, v2
	s_nop 1
	v_cndmask_b32_e32 v2, v2, v30, vcc
	v_cndmask_b32_e64 v4, v4, 27, vcc
	v_cmp_gt_f32_e32 vcc, v35, v2
	s_nop 1
	v_cndmask_b32_e32 v2, v2, v35, vcc
	v_cndmask_b32_e64 v4, v4, 28, vcc
	v_cmp_gt_f32_e32 vcc, v3, v2
	s_nop 1
	v_cndmask_b32_e32 v2, v2, v3, vcc
	v_cndmask_b32_e64 v4, v4, 29, vcc
	v_cmp_gt_f32_e32 vcc, v36, v2
	s_nop 1
	v_cndmask_b32_e32 v2, v2, v36, vcc
	v_cndmask_b32_e64 v4, v4, 30, vcc
	v_cmp_gt_f32_e32 vcc, v5, v2
	s_nop 1
	v_cndmask_b32_e32 v37, v2, v5, vcc
	v_cndmask_b32_e64 v2, v4, 31, vcc
	v_cmp_eq_u32_e32 vcc, 0, v2
	s_or_b64 vcc, vcc, s[10:11]
	v_cmp_eq_u32_e64 s[10:11], 1, v2
	v_cndmask_b32_e32 v4, v11, v82, vcc
	v_cmp_ngt_f32_e64 s[12:13], v9, v4
	s_or_b64 s[12:13], s[10:11], s[12:13]
	s_xor_b64 s[0:1], s[12:13], -1
	v_cndmask_b32_e64 v4, v9, v4, s[12:13]
	v_cndmask_b32_e64 v6, 0, 1, s[0:1]
	v_cmp_eq_u32_e64 s[0:1], 2, v2
	v_cmp_ngt_f32_e64 s[14:15], v8, v4
	s_or_b64 s[14:15], s[0:1], s[14:15]
	v_cmp_eq_u32_e64 s[2:3], 3, v2
	v_cndmask_b32_e64 v4, v8, v4, s[14:15]
	v_cmp_ngt_f32_e64 s[16:17], v7, v4
	s_or_b64 s[16:17], s[2:3], s[16:17]
	v_cndmask_b32_e64 v6, 2, v6, s[14:15]
	v_cndmask_b32_e64 v4, v7, v4, s[16:17]
	v_cndmask_b32_e64 v6, 3, v6, s[16:17]
	v_cmp_eq_u32_e64 s[16:17], 4, v2
	v_cmp_ngt_f32_e64 s[18:19], v15, v4
	s_or_b64 s[18:19], s[16:17], s[18:19]
	v_cmp_eq_u32_e64 s[72:73], 29, v2
	v_cndmask_b32_e64 v4, v15, v4, s[18:19]
	v_cndmask_b32_e64 v6, 4, v6, s[18:19]
	v_cmp_eq_u32_e64 s[18:19], 5, v2
	v_cmp_ngt_f32_e64 s[20:21], v13, v4
	s_or_b64 s[20:21], s[18:19], s[20:21]
	v_cmp_eq_u32_e64 s[70:71], 30, v2
	v_cndmask_b32_e64 v4, v13, v4, s[20:21]
	v_cndmask_b32_e64 v6, 5, v6, s[20:21]
	v_cmp_eq_u32_e64 s[20:21], 6, v2
	v_cmp_ngt_f32_e64 s[22:23], v12, v4
	s_or_b64 s[22:23], s[20:21], s[22:23]
	s_nop 0
	v_cndmask_b32_e64 v4, v12, v4, s[22:23]
; __device__ __forceinline__ void p7_ffn_prep(const Ctx& C, bool dummy = false) {
;     ...
;             for (int k = 0; k < 4; ++k) { float best = -__builtin_inff(); int be = 0;
; #pragma unroll
;                 for (int e = 0; e < 32; ++e) { const bool taken = (k > 0 && e == e4[0]) || (k > 1 && e == e4[1]) || (k > 2 && e == e4[2]); if (!taken && v[e] > best) { best = v[e]; be = e; } }
;                 e4[k] = be; tv[k] = best; }
	v_cndmask_b32_e64 v6, 6, v6, s[22:23]
	v_cmp_eq_u32_e64 s[22:23], 7, v2
	v_cmp_ngt_f32_e64 s[24:25], v10, v4
	s_or_b64 s[24:25], s[22:23], s[24:25]
	s_nop 0
	v_cndmask_b32_e64 v4, v10, v4, s[24:25]
	v_cndmask_b32_e64 v6, 7, v6, s[24:25]
	v_cmp_eq_u32_e64 s[24:25], 8, v2
	v_cmp_ngt_f32_e64 s[26:27], v19, v4
	s_or_b64 s[26:27], s[24:25], s[26:27]
	s_nop 0
	v_cndmask_b32_e64 v4, v19, v4, s[26:27]
	v_cndmask_b32_e64 v6, 8, v6, s[26:27]
	v_cmp_eq_u32_e64 s[26:27], 9, v2
	v_cmp_ngt_f32_e64 s[28:29], v17, v4
	s_or_b64 s[28:29], s[26:27], s[28:29]
	s_nop 0
	v_cndmask_b32_e64 v4, v17, v4, s[28:29]
	v_cndmask_b32_e64 v6, 9, v6, s[28:29]
	v_cmp_eq_u32_e64 s[28:29], 10, v2
	v_cmp_ngt_f32_e64 s[30:31], v16, v4
	s_or_b64 s[30:31], s[28:29], s[30:31]
	s_nop 0
	v_cndmask_b32_e64 v4, v16, v4, s[30:31]
	v_cndmask_b32_e64 v6, 10, v6, s[30:31]
	v_cmp_eq_u32_e64 s[30:31], 11, v2
	v_cmp_ngt_f32_e64 s[34:35], v14, v4
	s_or_b64 s[34:35], s[30:31], s[34:35]
	s_nop 0
	v_cndmask_b32_e64 v4, v14, v4, s[34:35]
	v_cndmask_b32_e64 v6, 11, v6, s[34:35]
	v_cmp_eq_u32_e64 s[34:35], 12, v2
	v_cmp_ngt_f32_e64 s[36:37], v23, v4
	s_or_b64 s[36:37], s[34:35], s[36:37]
	s_nop 0
	v_cndmask_b32_e64 v4, v23, v4, s[36:37]
	v_cndmask_b32_e64 v6, 12, v6, s[36:37]
	v_cmp_eq_u32_e64 s[36:37], 13, v2
	v_cmp_ngt_f32_e64 s[38:39], v21, v4
	s_or_b64 s[38:39], s[36:37], s[38:39]
	s_nop 0
	v_cndmask_b32_e64 v4, v21, v4, s[38:39]
	v_cndmask_b32_e64 v6, 13, v6, s[38:39]
	v_cmp_eq_u32_e64 s[38:39], 14, v2
	v_cmp_ngt_f32_e64 s[40:41], v20, v4
	s_or_b64 s[40:41], s[38:39], s[40:41]
	s_nop 0
	v_cndmask_b32_e64 v4, v20, v4, s[40:41]
	v_cndmask_b32_e64 v6, 14, v6, s[40:41]
	v_cmp_eq_u32_e64 s[40:41], 15, v2
	v_cmp_ngt_f32_e64 s[42:43], v18, v4
	s_or_b64 s[42:43], s[40:41], s[42:43]
	s_nop 0
	v_cndmask_b32_e64 v4, v18, v4, s[42:43]
	v_cndmask_b32_e64 v6, 15, v6, s[42:43]
	v_cmp_eq_u32_e64 s[42:43], 16, v2
	v_cmp_ngt_f32_e64 s[44:45], v27, v4
	s_or_b64 s[44:45], s[42:43], s[44:45]
	s_nop 0
	v_cndmask_b32_e64 v4, v27, v4, s[44:45]
	v_cndmask_b32_e64 v6, 16, v6, s[44:45]
	v_cmp_eq_u32_e64 s[44:45], 17, v2
	v_cmp_ngt_f32_e64 s[46:47], v25, v4
	s_or_b64 s[46:47], s[44:45], s[46:47]
	s_nop 0
	v_cndmask_b32_e64 v4, v25, v4, s[46:47]
	v_cndmask_b32_e64 v6, 17, v6, s[46:47]
	v_cmp_eq_u32_e64 s[46:47], 18, v2
	v_cmp_ngt_f32_e64 s[48:49], v24, v4
	s_or_b64 s[48:49], s[46:47], s[48:49]
	s_nop 0
	v_cndmask_b32_e64 v4, v24, v4, s[48:49]
	v_cndmask_b32_e64 v6, 18, v6, s[48:49]
	v_cmp_eq_u32_e64 s[48:49], 19, v2
	v_cmp_ngt_f32_e64 s[50:51], v22, v4
	s_or_b64 s[50:51], s[48:49], s[50:51]
	s_nop 0
	v_cndmask_b32_e64 v4, v22, v4, s[50:51]
	v_cndmask_b32_e64 v6, 19, v6, s[50:51]
	v_cmp_eq_u32_e64 s[50:51], 20, v2
	v_cmp_ngt_f32_e64 s[52:53], v31, v4
	s_or_b64 s[52:53], s[50:51], s[52:53]
	s_nop 0
	v_cndmask_b32_e64 v4, v31, v4, s[52:53]
	v_cndmask_b32_e64 v6, 20, v6, s[52:53]
	v_cmp_eq_u32_e64 s[52:53], 21, v2
	v_cmp_ngt_f32_e64 s[54:55], v29, v4
	s_or_b64 s[54:55], s[52:53], s[54:55]
	s_nop 0
	v_cndmask_b32_e64 v4, v29, v4, s[54:55]
	v_cndmask_b32_e64 v6, 21, v6, s[54:55]
	v_cmp_eq_u32_e64 s[54:55], 22, v2
	v_cmp_ngt_f32_e64 s[56:57], v28, v4
	s_or_b64 s[56:57], s[54:55], s[56:57]
	s_nop 0
	v_cndmask_b32_e64 v4, v28, v4, s[56:57]
	v_cndmask_b32_e64 v6, 22, v6, s[56:57]
	v_cmp_eq_u32_e64 s[56:57], 23, v2
	v_cmp_ngt_f32_e64 s[58:59], v26, v4
	s_or_b64 s[58:59], s[56:57], s[58:59]
	s_nop 0
	v_cndmask_b32_e64 v4, v26, v4, s[58:59]
	v_cndmask_b32_e64 v6, 23, v6, s[58:59]
	v_cmp_eq_u32_e64 s[58:59], 24, v2
	v_cmp_ngt_f32_e64 s[60:61], v34, v4
	s_or_b64 s[60:61], s[58:59], s[60:61]
	s_nop 0
	v_cndmask_b32_e64 v4, v34, v4, s[60:61]
	v_cndmask_b32_e64 v6, 24, v6, s[60:61]
	v_cmp_eq_u32_e64 s[60:61], 25, v2
	v_cmp_ngt_f32_e64 s[62:63], v33, v4
	s_or_b64 s[62:63], s[60:61], s[62:63]
	s_nop 0
	v_cndmask_b32_e64 v4, v33, v4, s[62:63]
	v_cndmask_b32_e64 v6, 25, v6, s[62:63]
	v_cmp_eq_u32_e64 s[62:63], 26, v2
	v_cmp_ngt_f32_e64 s[64:65], v32, v4
	s_or_b64 s[64:65], s[62:63], s[64:65]
	s_nop 0
	v_cndmask_b32_e64 v4, v32, v4, s[64:65]
	v_cndmask_b32_e64 v6, 26, v6, s[64:65]
	v_cmp_eq_u32_e64 s[64:65], 27, v2
	v_cmp_ngt_f32_e64 s[66:67], v30, v4
	s_or_b64 s[66:67], s[64:65], s[66:67]
	s_nop 0
	v_cndmask_b32_e64 v4, v30, v4, s[66:67]
	v_cndmask_b32_e64 v6, 27, v6, s[66:67]
	v_cmp_eq_u32_e64 s[66:67], 28, v2
	v_cmp_ngt_f32_e64 s[68:69], v35, v4
	s_or_b64 s[68:69], s[66:67], s[68:69]
	s_nop 0
	v_cndmask_b32_e64 v4, v35, v4, s[68:69]
	v_cndmask_b32_e64 v6, 28, v6, s[68:69]
	v_cmp_ngt_f32_e64 s[68:69], v3, v4
	s_or_b64 s[68:69], s[72:73], s[68:69]
	s_nop 0
	v_cndmask_b32_e64 v4, v3, v4, s[68:69]
	v_cndmask_b32_e64 v6, 29, v6, s[68:69]
	v_cmp_ngt_f32_e64 s[68:69], v36, v4
	s_or_b64 s[68:69], s[70:71], s[68:69]
	s_nop 0
	v_cndmask_b32_e64 v4, v36, v4, s[68:69]
	v_cndmask_b32_e64 v6, 30, v6, s[68:69]
	v_cmp_eq_u32_e64 s[68:69], 31, v2
	v_cmp_ngt_f32_e64 s[74:75], v5, v4
	s_or_b64 s[74:75], s[68:69], s[74:75]
	s_nop 0
	v_cndmask_b32_e64 v38, v5, v4, s[74:75]
	v_cndmask_b32_e64 v4, 31, v6, s[74:75]
	v_cmp_eq_u32_e64 s[74:75], 0, v4
	s_or_b64 vcc, vcc, s[74:75]
	v_cndmask_b32_e32 v6, v11, v82, vcc
	v_cmp_eq_u32_e64 s[74:75], 1, v4
	s_or_b64 s[12:13], s[10:11], s[74:75]
	v_cmp_ngt_f32_e64 s[10:11], v9, v6
	s_or_b64 s[10:11], s[12:13], s[10:11]
	s_xor_b64 s[4:5], s[10:11], -1
	v_cndmask_b32_e64 v6, v9, v6, s[10:11]
	v_cmp_eq_u32_e64 s[10:11], 2, v4
	s_or_b64 s[14:15], s[0:1], s[10:11]
	v_cmp_ngt_f32_e64 s[10:11], v8, v6
	v_cndmask_b32_e64 v39, 0, 1, s[4:5]
	s_or_b64 s[10:11], s[14:15], s[10:11]
	v_cndmask_b32_e64 v6, v8, v6, s[10:11]
	v_cndmask_b32_e64 v39, 2, v39, s[10:11]
	v_cmp_eq_u32_e64 s[10:11], 3, v4
	s_or_b64 s[78:79], s[2:3], s[10:11]
; __device__ __forceinline__ void p7_ffn_prep(const Ctx& C, bool dummy = false) {
;     ...
;             for (int k = 0; k < 4; ++k) { float best = -__builtin_inff(); int be = 0;
; #pragma unroll
;                 for (int e = 0; e < 32; ++e) { const bool taken = (k > 0 && e == e4[0]) || (k > 1 && e == e4[1]) || (k > 2 && e == e4[2]); if (!taken && v[e] > best) { best = v[e]; be = e; } }
;                 e4[k] = be; tv[k] = best; }
	v_cmp_ngt_f32_e64 s[10:11], v7, v6
	s_or_b64 s[10:11], s[78:79], s[10:11]
	s_nop 0
	v_cndmask_b32_e64 v6, v7, v6, s[10:11]
	v_cndmask_b32_e64 v39, 3, v39, s[10:11]
	v_cmp_eq_u32_e64 s[10:11], 4, v4
	s_or_b64 s[76:77], s[16:17], s[10:11]
	v_cmp_ngt_f32_e64 s[10:11], v15, v6
	s_or_b64 s[10:11], s[76:77], s[10:11]
	s_nop 0
	v_cndmask_b32_e64 v6, v15, v6, s[10:11]
	v_cndmask_b32_e64 v39, 4, v39, s[10:11]
	v_cmp_eq_u32_e64 s[10:11], 5, v4
	s_or_b64 s[0:1], s[18:19], s[10:11]
	v_cmp_ngt_f32_e64 s[10:11], v13, v6
	s_or_b64 s[10:11], s[0:1], s[10:11]
	s_xor_b64 s[0:1], s[0:1], -1
	v_cndmask_b32_e64 v6, v13, v6, s[10:11]
	v_cndmask_b32_e64 v39, 5, v39, s[10:11]
	v_cmp_eq_u32_e64 s[10:11], 6, v4
	s_or_b64 s[2:3], s[20:21], s[10:11]
	v_cmp_ngt_f32_e64 s[10:11], v12, v6
	s_or_b64 s[10:11], s[2:3], s[10:11]
	s_nop 0
	v_cndmask_b32_e64 v6, v12, v6, s[10:11]
	v_cndmask_b32_e64 v39, 6, v39, s[10:11]
	v_cmp_eq_u32_e64 s[10:11], 7, v4
	s_or_b64 s[96:97], s[22:23], s[10:11]
	v_cmp_ngt_f32_e64 s[10:11], v10, v6
	s_or_b64 s[10:11], s[96:97], s[10:11]
	s_nop 0
	v_cndmask_b32_e64 v6, v10, v6, s[10:11]
	v_cndmask_b32_e64 v39, 7, v39, s[10:11]
	v_cmp_eq_u32_e64 s[10:11], 8, v4
	s_or_b64 s[94:95], s[24:25], s[10:11]
	v_cmp_ngt_f32_e64 s[10:11], v19, v6
	s_or_b64 s[10:11], s[94:95], s[10:11]
	s_nop 0
	v_cndmask_b32_e64 v6, v19, v6, s[10:11]
	v_cndmask_b32_e64 v39, 8, v39, s[10:11]
	v_cmp_eq_u32_e64 s[10:11], 9, v4
	s_or_b64 s[8:9], s[26:27], s[10:11]
	v_cmp_ngt_f32_e64 s[10:11], v17, v6
	s_or_b64 s[10:11], s[8:9], s[10:11]
	s_nop 0
	v_cndmask_b32_e64 v6, v17, v6, s[10:11]
	v_cndmask_b32_e64 v39, 9, v39, s[10:11]
	v_cmp_eq_u32_e64 s[10:11], 10, v4
	s_or_b64 s[6:7], s[28:29], s[10:11]
	v_cmp_ngt_f32_e64 s[10:11], v16, v6
	s_or_b64 s[10:11], s[6:7], s[10:11]
	s_nop 0
	v_cndmask_b32_e64 v6, v16, v6, s[10:11]
	v_cndmask_b32_e64 v39, 10, v39, s[10:11]
	v_cmp_eq_u32_e64 s[10:11], 11, v4
	s_or_b64 s[80:81], s[30:31], s[10:11]
	v_cmp_ngt_f32_e64 s[10:11], v14, v6
	s_or_b64 s[10:11], s[80:81], s[10:11]
	s_nop 0
	v_cndmask_b32_e64 v6, v14, v6, s[10:11]
	v_cndmask_b32_e64 v39, 11, v39, s[10:11]
	v_cmp_eq_u32_e64 s[10:11], 12, v4
	s_or_b64 s[92:93], s[34:35], s[10:11]
	v_cmp_ngt_f32_e64 s[10:11], v23, v6
	s_or_b64 s[10:11], s[92:93], s[10:11]
	s_nop 0
	v_cndmask_b32_e64 v6, v23, v6, s[10:11]
	v_cndmask_b32_e64 v39, 12, v39, s[10:11]
	v_cmp_eq_u32_e64 s[10:11], 13, v4
	s_or_b64 s[18:19], s[36:37], s[10:11]
	v_cmp_ngt_f32_e64 s[10:11], v21, v6
	s_or_b64 s[10:11], s[18:19], s[10:11]
	s_nop 0
	v_cndmask_b32_e64 v6, v21, v6, s[10:11]
	v_cndmask_b32_e64 v39, 13, v39, s[10:11]
	v_cmp_eq_u32_e64 s[10:11], 14, v4
	s_or_b64 s[4:5], s[38:39], s[10:11]
	v_cmp_ngt_f32_e64 s[10:11], v20, v6
	s_or_b64 s[10:11], s[4:5], s[10:11]
	s_nop 0
	v_cndmask_b32_e64 v6, v20, v6, s[10:11]
	v_cndmask_b32_e64 v39, 14, v39, s[10:11]
	v_cmp_eq_u32_e64 s[10:11], 15, v4
	s_or_b64 s[16:17], s[40:41], s[10:11]
	v_cmp_ngt_f32_e64 s[10:11], v18, v6
	s_or_b64 s[10:11], s[16:17], s[10:11]
	s_nop 0
	v_cndmask_b32_e64 v6, v18, v6, s[10:11]
	v_cndmask_b32_e64 v39, 15, v39, s[10:11]
	v_cmp_eq_u32_e64 s[10:11], 16, v4
	s_or_b64 s[74:75], s[42:43], s[10:11]
	v_cmp_ngt_f32_e64 s[10:11], v27, v6
	s_or_b64 s[10:11], s[74:75], s[10:11]
	s_nop 0
	v_cndmask_b32_e64 v6, v27, v6, s[10:11]
	v_cndmask_b32_e64 v39, 16, v39, s[10:11]
	v_cmp_eq_u32_e64 s[10:11], 17, v4
	s_or_b64 s[42:43], s[44:45], s[10:11]
	v_cmp_ngt_f32_e64 s[10:11], v25, v6
	s_or_b64 s[10:11], s[42:43], s[10:11]
	s_nop 0
	v_cndmask_b32_e64 v6, v25, v6, s[10:11]
	v_cndmask_b32_e64 v39, 17, v39, s[10:11]
	v_cmp_eq_u32_e64 s[10:11], 18, v4
	s_or_b64 s[40:41], s[46:47], s[10:11]
	v_cmp_ngt_f32_e64 s[10:11], v24, v6
	s_or_b64 s[10:11], s[40:41], s[10:11]
	s_nop 0
	v_cndmask_b32_e64 v6, v24, v6, s[10:11]
	v_cndmask_b32_e64 v39, 18, v39, s[10:11]
	v_cmp_eq_u32_e64 s[10:11], 19, v4
	s_or_b64 s[38:39], s[48:49], s[10:11]
	v_cmp_ngt_f32_e64 s[10:11], v22, v6
	s_or_b64 s[10:11], s[38:39], s[10:11]
	s_nop 0
	v_cndmask_b32_e64 v6, v22, v6, s[10:11]
	v_cndmask_b32_e64 v39, 19, v39, s[10:11]
	v_cmp_eq_u32_e64 s[10:11], 20, v4
	s_or_b64 s[36:37], s[50:51], s[10:11]
	v_cmp_ngt_f32_e64 s[10:11], v31, v6
	s_or_b64 s[10:11], s[36:37], s[10:11]
	s_nop 0
	v_cndmask_b32_e64 v6, v31, v6, s[10:11]
	v_cndmask_b32_e64 v39, 20, v39, s[10:11]
	v_cmp_eq_u32_e64 s[10:11], 21, v4
	s_or_b64 s[34:35], s[52:53], s[10:11]
	v_cmp_ngt_f32_e64 s[10:11], v29, v6
	s_or_b64 s[10:11], s[34:35], s[10:11]
	s_nop 0
	v_cndmask_b32_e64 v6, v29, v6, s[10:11]
	v_cndmask_b32_e64 v39, 21, v39, s[10:11]
	v_cmp_eq_u32_e64 s[10:11], 22, v4
	s_or_b64 s[30:31], s[54:55], s[10:11]
	v_cmp_ngt_f32_e64 s[10:11], v28, v6
	s_or_b64 s[10:11], s[30:31], s[10:11]
	s_nop 0
	v_cndmask_b32_e64 v6, v28, v6, s[10:11]
	v_cndmask_b32_e64 v39, 22, v39, s[10:11]
	v_cmp_eq_u32_e64 s[10:11], 23, v4
	s_or_b64 s[28:29], s[56:57], s[10:11]
	v_cmp_ngt_f32_e64 s[10:11], v26, v6
	s_or_b64 s[10:11], s[28:29], s[10:11]
	s_nop 0
	v_cndmask_b32_e64 v6, v26, v6, s[10:11]
	v_cndmask_b32_e64 v39, 23, v39, s[10:11]
	v_cmp_eq_u32_e64 s[10:11], 24, v4
	s_or_b64 s[26:27], s[58:59], s[10:11]
	v_cmp_ngt_f32_e64 s[10:11], v34, v6
	s_or_b64 s[10:11], s[26:27], s[10:11]
	s_nop 0
	v_cndmask_b32_e64 v6, v34, v6, s[10:11]
	v_cndmask_b32_e64 v39, 24, v39, s[10:11]
	v_cmp_eq_u32_e64 s[10:11], 25, v4
	s_or_b64 s[24:25], s[60:61], s[10:11]
	v_cmp_ngt_f32_e64 s[10:11], v33, v6
	s_or_b64 s[10:11], s[24:25], s[10:11]
	s_nop 0
	v_cndmask_b32_e64 v6, v33, v6, s[10:11]
	v_cndmask_b32_e64 v39, 25, v39, s[10:11]
	v_cmp_eq_u32_e64 s[10:11], 26, v4
	s_or_b64 s[22:23], s[62:63], s[10:11]
	v_cmp_ngt_f32_e64 s[10:11], v32, v6
	s_or_b64 s[10:11], s[22:23], s[10:11]
; __device__ __forceinline__ void p7_ffn_prep(const Ctx& C, bool dummy = false) {
;     ...
;             for (int k = 0; k < 4; ++k) { float best = -__builtin_inff(); int be = 0;
; #pragma unroll
;                 for (int e = 0; e < 32; ++e) { const bool taken = (k > 0 && e == e4[0]) || (k > 1 && e == e4[1]) || (k > 2 && e == e4[2]); if (!taken && v[e] > best) { best = v[e]; be = e; } }
;                 e4[k] = be; tv[k] = best; }
	v_readlane_b32 s60, v254, 8
	v_cndmask_b32_e64 v6, v32, v6, s[10:11]
	v_cndmask_b32_e64 v39, 26, v39, s[10:11]
	v_cmp_eq_u32_e64 s[10:11], 27, v4
	s_or_b64 s[20:21], s[64:65], s[10:11]
	v_cmp_ngt_f32_e64 s[10:11], v30, v6
	s_or_b64 s[10:11], s[20:21], s[10:11]
	v_readlane_b32 s61, v254, 9
	v_cndmask_b32_e64 v6, v30, v6, s[10:11]
	v_cndmask_b32_e64 v39, 27, v39, s[10:11]
	v_cmp_eq_u32_e64 s[10:11], 28, v4
	s_or_b64 s[50:51], s[66:67], s[10:11]
	v_cmp_ngt_f32_e64 s[10:11], v35, v6
	s_or_b64 s[10:11], s[50:51], s[10:11]
	v_readlane_b32 s62, v254, 10
	v_cndmask_b32_e64 v6, v35, v6, s[10:11]
	v_cndmask_b32_e64 v39, 28, v39, s[10:11]
	v_cmp_eq_u32_e64 s[10:11], 29, v4
	s_or_b64 s[48:49], s[72:73], s[10:11]
	v_cmp_ngt_f32_e64 s[10:11], v3, v6
	s_or_b64 s[10:11], s[48:49], s[10:11]
	v_readlane_b32 s63, v254, 11
	v_cndmask_b32_e64 v6, v3, v6, s[10:11]
	v_cndmask_b32_e64 v39, 29, v39, s[10:11]
	v_cmp_eq_u32_e64 s[10:11], 30, v4
	s_or_b64 s[46:47], s[70:71], s[10:11]
	v_cmp_ngt_f32_e64 s[10:11], v36, v6
	s_or_b64 s[10:11], s[46:47], s[10:11]
	s_nop 0
	v_cndmask_b32_e64 v6, v36, v6, s[10:11]
	v_cndmask_b32_e64 v39, 30, v39, s[10:11]
	v_cmp_eq_u32_e64 s[10:11], 31, v4
	s_or_b64 s[44:45], s[68:69], s[10:11]
	v_cmp_ngt_f32_e64 s[10:11], v5, v6
	s_or_b64 s[10:11], s[44:45], s[10:11]
	s_nop 0
	v_cndmask_b32_e64 v40, v5, v6, s[10:11]
	v_cndmask_b32_e64 v6, 31, v39, s[10:11]
	v_cmp_eq_u32_e64 s[10:11], 0, v6
	s_or_b64 vcc, vcc, s[10:11]
	v_cndmask_b32_e32 v11, v11, v82, vcc
	v_cmp_ne_u32_e32 vcc, 1, v6
	s_xor_b64 s[10:11], s[12:13], -1
	s_and_b64 s[10:11], s[10:11], vcc
	v_cmp_gt_f32_e32 vcc, v9, v11
	s_and_b64 vcc, s[10:11], vcc
	s_xor_b64 s[10:11], s[14:15], -1
	v_cndmask_b32_e32 v9, v11, v9, vcc
	v_cndmask_b32_e64 v11, 0, 1, vcc
	v_cmp_ne_u32_e32 vcc, 2, v6
	s_and_b64 s[10:11], s[10:11], vcc
	v_cmp_gt_f32_e32 vcc, v8, v9
	s_and_b64 vcc, s[10:11], vcc
	s_xor_b64 s[10:11], s[78:79], -1
	v_cndmask_b32_e32 v8, v9, v8, vcc
	v_cndmask_b32_e64 v9, v11, 2, vcc
	v_cmp_ne_u32_e32 vcc, 3, v6
	s_and_b64 s[10:11], s[10:11], vcc
	v_cmp_gt_f32_e32 vcc, v7, v8
	s_and_b64 vcc, s[10:11], vcc
	s_xor_b64 s[10:11], s[76:77], -1
	v_cndmask_b32_e32 v7, v8, v7, vcc
	v_cndmask_b32_e64 v8, v9, 3, vcc
	v_cmp_ne_u32_e32 vcc, 4, v6
	s_and_b64 s[10:11], s[10:11], vcc
	v_cmp_gt_f32_e32 vcc, v15, v7
	s_and_b64 vcc, s[10:11], vcc
	s_nop 0
	v_cndmask_b32_e32 v7, v7, v15, vcc
	v_cndmask_b32_e64 v8, v8, 4, vcc
	v_cmp_ne_u32_e32 vcc, 5, v6
	s_and_b64 s[0:1], s[0:1], vcc
	v_cmp_gt_f32_e32 vcc, v13, v7
	s_and_b64 vcc, s[0:1], vcc
	s_xor_b64 s[0:1], s[2:3], -1
	v_cndmask_b32_e32 v7, v7, v13, vcc
	v_cndmask_b32_e64 v8, v8, 5, vcc
	v_cmp_ne_u32_e32 vcc, 6, v6
	s_and_b64 s[0:1], s[0:1], vcc
	v_cmp_gt_f32_e32 vcc, v12, v7
	s_and_b64 vcc, s[0:1], vcc
	s_xor_b64 s[0:1], s[96:97], -1
	v_cndmask_b32_e32 v7, v7, v12, vcc
	v_cndmask_b32_e64 v8, v8, 6, vcc
	v_cmp_ne_u32_e32 vcc, 7, v6
	s_and_b64 s[0:1], s[0:1], vcc
	v_cmp_gt_f32_e32 vcc, v10, v7
	s_and_b64 vcc, s[0:1], vcc
	s_xor_b64 s[0:1], s[94:95], -1
	v_cndmask_b32_e32 v7, v7, v10, vcc
	v_cndmask_b32_e64 v8, v8, 7, vcc
	v_cmp_ne_u32_e32 vcc, 8, v6
	s_and_b64 s[0:1], s[0:1], vcc
	v_cmp_gt_f32_e32 vcc, v19, v7
	s_and_b64 vcc, s[0:1], vcc
	s_xor_b64 s[0:1], s[8:9], -1
	v_cndmask_b32_e32 v7, v7, v19, vcc
	v_cndmask_b32_e64 v8, v8, 8, vcc
	v_cmp_ne_u32_e32 vcc, 9, v6
	s_and_b64 s[0:1], s[0:1], vcc
	v_cmp_gt_f32_e32 vcc, v17, v7
	s_and_b64 vcc, s[0:1], vcc
	s_xor_b64 s[0:1], s[6:7], -1
	v_cndmask_b32_e32 v7, v7, v17, vcc
	v_cndmask_b32_e64 v8, v8, 9, vcc
	v_cmp_ne_u32_e32 vcc, 10, v6
	s_and_b64 s[0:1], s[0:1], vcc
	v_cmp_gt_f32_e32 vcc, v16, v7
	s_and_b64 vcc, s[0:1], vcc
	s_xor_b64 s[0:1], s[80:81], -1
	v_cndmask_b32_e32 v7, v7, v16, vcc
	v_cndmask_b32_e64 v8, v8, 10, vcc
	v_cmp_ne_u32_e32 vcc, 11, v6
	s_and_b64 s[0:1], s[0:1], vcc
	v_cmp_gt_f32_e32 vcc, v14, v7
	s_and_b64 vcc, s[0:1], vcc
	s_xor_b64 s[0:1], s[92:93], -1
	v_cndmask_b32_e32 v7, v7, v14, vcc
	v_cndmask_b32_e64 v8, v8, 11, vcc
	v_cmp_ne_u32_e32 vcc, 12, v6
	s_and_b64 s[0:1], s[0:1], vcc
	v_cmp_gt_f32_e32 vcc, v23, v7
	s_and_b64 vcc, s[0:1], vcc
	s_xor_b64 s[0:1], s[18:19], -1
	v_cndmask_b32_e32 v7, v7, v23, vcc
	v_cndmask_b32_e64 v8, v8, 12, vcc
	v_cmp_ne_u32_e32 vcc, 13, v6
	s_and_b64 s[0:1], s[0:1], vcc
	v_cmp_gt_f32_e32 vcc, v21, v7
	s_and_b64 vcc, s[0:1], vcc
	s_xor_b64 s[0:1], s[4:5], -1
	v_cndmask_b32_e32 v7, v7, v21, vcc
	v_cndmask_b32_e64 v8, v8, 13, vcc
	v_cmp_ne_u32_e32 vcc, 14, v6
	s_and_b64 s[0:1], s[0:1], vcc
	v_cmp_gt_f32_e32 vcc, v20, v7
	s_and_b64 vcc, s[0:1], vcc
	s_xor_b64 s[0:1], s[16:17], -1
	v_cndmask_b32_e32 v7, v7, v20, vcc
	v_cndmask_b32_e64 v8, v8, 14, vcc
	v_cmp_ne_u32_e32 vcc, 15, v6
	s_and_b64 s[0:1], s[0:1], vcc
; __device__ __forceinline__ void p7_ffn_prep(const Ctx& C, bool dummy = false) {
;     ...
;             for (int k = 0; k < 4; ++k) { float best = -__builtin_inff(); int be = 0;
; #pragma unroll
;                 for (int e = 0; e < 32; ++e) { const bool taken = (k > 0 && e == e4[0]) || (k > 1 && e == e4[1]) || (k > 2 && e == e4[2]); if (!taken && v[e] > best) { best = v[e]; be = e; } }
;                 e4[k] = be; tv[k] = best; }
;             const float p1 = __expf(tv[1] - tv[0]), p2 = __expf(tv[2] - tv[0]), p3 = __expf(tv[3] - tv[0]); const float inv = 1.0f / (1.0f + p1 + p2 + p3);
;             gk[0] = inv; gk[1] = p1 * inv; gk[2] = p2 * inv; gk[3] = p3 * inv;
; #pragma unroll
;             for (int k = 0; k < 4; ++k) rk[k] = __hip_atomic_fetch_add(cnt + e4[k], 1, __ATOMIC_RELAXED, __HIP_MEMORY_SCOPE_WORKGROUP);
	v_cmp_gt_f32_e32 vcc, v18, v7
	s_and_b64 vcc, s[0:1], vcc
	s_xor_b64 s[0:1], s[74:75], -1
	v_cndmask_b32_e32 v7, v7, v18, vcc
	v_cndmask_b32_e64 v8, v8, 15, vcc
	v_cmp_ne_u32_e32 vcc, 16, v6
	s_and_b64 s[0:1], s[0:1], vcc
	v_cmp_gt_f32_e32 vcc, v27, v7
	s_and_b64 vcc, s[0:1], vcc
	s_xor_b64 s[0:1], s[42:43], -1
	v_cndmask_b32_e32 v7, v7, v27, vcc
	v_cndmask_b32_e64 v8, v8, 16, vcc
	v_cmp_ne_u32_e32 vcc, 17, v6
	s_and_b64 s[0:1], s[0:1], vcc
	v_cmp_gt_f32_e32 vcc, v25, v7
	s_and_b64 vcc, s[0:1], vcc
	s_xor_b64 s[0:1], s[40:41], -1
	v_cndmask_b32_e32 v7, v7, v25, vcc
	v_cndmask_b32_e64 v8, v8, 17, vcc
	v_cmp_ne_u32_e32 vcc, 18, v6
	s_and_b64 s[0:1], s[0:1], vcc
	v_cmp_gt_f32_e32 vcc, v24, v7
	s_and_b64 vcc, s[0:1], vcc
	s_xor_b64 s[0:1], s[38:39], -1
	v_cndmask_b32_e32 v7, v7, v24, vcc
	v_cndmask_b32_e64 v8, v8, 18, vcc
	v_cmp_ne_u32_e32 vcc, 19, v6
	s_and_b64 s[0:1], s[0:1], vcc
	v_cmp_gt_f32_e32 vcc, v22, v7
	s_and_b64 vcc, s[0:1], vcc
	s_xor_b64 s[0:1], s[36:37], -1
	v_cndmask_b32_e32 v7, v7, v22, vcc
	v_cndmask_b32_e64 v8, v8, 19, vcc
	v_cmp_ne_u32_e32 vcc, 20, v6
	s_and_b64 s[0:1], s[0:1], vcc
	v_cmp_gt_f32_e32 vcc, v31, v7
	s_and_b64 vcc, s[0:1], vcc
	s_xor_b64 s[0:1], s[34:35], -1
	v_cndmask_b32_e32 v7, v7, v31, vcc
	v_cndmask_b32_e64 v8, v8, 20, vcc
	v_cmp_ne_u32_e32 vcc, 21, v6
	s_and_b64 s[0:1], s[0:1], vcc
	v_cmp_gt_f32_e32 vcc, v29, v7
	s_and_b64 vcc, s[0:1], vcc
	s_xor_b64 s[0:1], s[30:31], -1
	v_cndmask_b32_e32 v7, v7, v29, vcc
	v_cndmask_b32_e64 v8, v8, 21, vcc
	v_cmp_ne_u32_e32 vcc, 22, v6
	s_and_b64 s[0:1], s[0:1], vcc
	v_cmp_gt_f32_e32 vcc, v28, v7
	s_and_b64 vcc, s[0:1], vcc
	s_xor_b64 s[0:1], s[28:29], -1
	v_cndmask_b32_e32 v7, v7, v28, vcc
	v_cndmask_b32_e64 v8, v8, 22, vcc
	v_cmp_ne_u32_e32 vcc, 23, v6
	s_and_b64 s[0:1], s[0:1], vcc
	v_cmp_gt_f32_e32 vcc, v26, v7
	s_and_b64 vcc, s[0:1], vcc
	s_xor_b64 s[0:1], s[26:27], -1
	v_cndmask_b32_e32 v7, v7, v26, vcc
	v_cndmask_b32_e64 v8, v8, 23, vcc
	v_cmp_ne_u32_e32 vcc, 24, v6
	s_and_b64 s[0:1], s[0:1], vcc
	v_cmp_gt_f32_e32 vcc, v34, v7
	s_and_b64 vcc, s[0:1], vcc
	s_xor_b64 s[0:1], s[24:25], -1
	v_cndmask_b32_e32 v7, v7, v34, vcc
	v_cndmask_b32_e64 v8, v8, 24, vcc
	v_cmp_ne_u32_e32 vcc, 25, v6
	s_and_b64 s[0:1], s[0:1], vcc
	v_cmp_gt_f32_e32 vcc, v33, v7
	s_and_b64 vcc, s[0:1], vcc
	s_xor_b64 s[0:1], s[22:23], -1
	v_cndmask_b32_e32 v7, v7, v33, vcc
	v_cndmask_b32_e64 v8, v8, 25, vcc
	v_cmp_ne_u32_e32 vcc, 26, v6
	s_and_b64 s[0:1], s[0:1], vcc
	v_cmp_gt_f32_e32 vcc, v32, v7
	s_and_b64 vcc, s[0:1], vcc
	s_xor_b64 s[0:1], s[20:21], -1
	v_cndmask_b32_e32 v7, v7, v32, vcc
	v_cndmask_b32_e64 v8, v8, 26, vcc
	v_cmp_ne_u32_e32 vcc, 27, v6
	s_and_b64 s[0:1], s[0:1], vcc
	v_cmp_gt_f32_e32 vcc, v30, v7
	s_and_b64 vcc, s[0:1], vcc
	s_xor_b64 s[0:1], s[50:51], -1
	v_cndmask_b32_e32 v7, v7, v30, vcc
	v_cndmask_b32_e64 v8, v8, 27, vcc
	v_cmp_ne_u32_e32 vcc, 28, v6
	s_and_b64 s[0:1], s[0:1], vcc
	v_cmp_gt_f32_e32 vcc, v35, v7
	s_and_b64 vcc, s[0:1], vcc
	s_xor_b64 s[0:1], s[48:49], -1
	v_cndmask_b32_e32 v7, v7, v35, vcc
	v_cndmask_b32_e64 v8, v8, 28, vcc
	v_cmp_ne_u32_e32 vcc, 29, v6
	s_and_b64 s[0:1], s[0:1], vcc
	v_cmp_gt_f32_e32 vcc, v3, v7
	s_and_b64 vcc, s[0:1], vcc
	s_xor_b64 s[0:1], s[46:47], -1
	v_cndmask_b32_e32 v3, v7, v3, vcc
	v_cndmask_b32_e64 v7, v8, 29, vcc
	v_cmp_ne_u32_e32 vcc, 30, v6
	s_and_b64 s[0:1], s[0:1], vcc
	v_cmp_gt_f32_e32 vcc, v36, v3
	s_and_b64 vcc, s[0:1], vcc
	s_xor_b64 s[0:1], s[44:45], -1
	v_cndmask_b32_e32 v3, v3, v36, vcc
	v_cndmask_b32_e64 v7, v7, 30, vcc
	v_cmp_ne_u32_e32 vcc, 31, v6
	s_and_b64 s[0:1], s[0:1], vcc
	v_cmp_gt_f32_e32 vcc, v5, v3
	s_and_b64 vcc, s[0:1], vcc
	s_nop 0
	v_cndmask_b32_e32 v3, v3, v5, vcc
	v_sub_f32_e32 v5, v38, v37
	v_mul_f32_e32 v5, 0x3fb8aa3b, v5
	v_exp_f32_e32 v10, v5
	v_sub_f32_e32 v5, v40, v37
	v_mul_f32_e32 v5, 0x3fb8aa3b, v5
	v_sub_f32_e32 v3, v3, v37
	v_exp_f32_e32 v11, v5
	v_mul_f32_e32 v3, 0x3fb8aa3b, v3
	v_exp_f32_e32 v3, v3
	v_add_f32_e32 v5, 1.0, v10
	v_add_f32_e32 v5, v5, v11
	v_cndmask_b32_e64 v8, v7, 31, vcc
	v_add_f32_e32 v5, v5, v3
	v_div_scale_f32 v7, s[0:1], v5, v5, 1.0
	v_rcp_f32_e32 v9, v7
	s_nop 0
	v_fma_f32 v12, -v7, v9, 1.0
	v_fmac_f32_e32 v9, v12, v9
	v_div_scale_f32 v12, vcc, 1.0, v5, 1.0
	v_mul_f32_e32 v13, v12, v9
	v_fma_f32 v14, -v7, v13, v12
	v_fmac_f32_e32 v13, v14, v9
	v_fma_f32 v7, -v7, v13, v12
	v_div_fmas_f32 v7, v7, v9, v13
	v_div_fixup_f32 v12, v7, v5, 1.0
	v_pk_mul_f32 v[10:11], v[10:11], v[12:13] op_sel_hi:[1,0]
	v_mul_f32_e32 v13, v3, v12
	v_lshl_add_u32 v3, v2, 2, 0
	ds_add_rtn_u32 v20, v3, v80
	v_lshl_add_u32 v3, v4, 2, 0
	ds_add_rtn_u32 v18, v3, v80
	v_lshl_add_u32 v3, v6, 2, 0
	ds_add_rtn_u32 v16, v3, v80
	v_lshl_add_u32 v3, v8, 2, 0
	ds_add_rtn_u32 v14, v3, v80
